# rstd partial-sum loads de-serialised in all four epilogues (in-proj fp8+bf16, dense-up bf16+fp8)
# baseline (speedup 1.0000x reference)
; __device__ __forceinline__ float rstd_q(const float* ssq, int row, int fq) {
;     const f32x4 p = *(const f32x4*)(ssq + 16 * (size_t)row + 4 * fq); float s = (p.x + p.y) + (p.z + p.w); s += swz_f<16>(s); s = sum_x32(s);
;     return __builtin_amdgcn_rsqf(s * (1.f / 1024.f) + EPS);
;     __device__ __forceinline__ void operator()(const f32x4 (&acc)[2][2][4][2], const Unit& u, int wr, int wc, int fr, int fq) const {
;         const int pn = u.pn + pn_off, type = GATES ? (pn < 14 ? 3 : 4) : (pn < 4 ? 0 : pn == 4 ? 1 : pn < 10 ? 2 : pn < 14 ? 3 : 4);
;         const float* gp = (type == 0 ? qg : kg) + 8 * fq; const float gsc = type == 0 ? QSCALE : 1.f;
;         float rs8[2][4];
; #pragma unroll
;         for (int ai = 0; ai < 2; ++ai)
; #pragma unroll
;             for (int m = 0; m < 4; ++m) rs8[ai][m] = rstd_q(ssq, EPI_ROWS(ai, m), fq) * ascale;
; #pragma unroll
;         for (int ai = 0; ai < 2; ++ai)
; #pragma unroll
;             for (int m = 0; m < 4; ++m) { const int row = EPI_ROWS(ai, m); const float rs = rs8[ai][m]; f32x4 v[2][2];
; #pragma unroll
;                 for (int bj = 0; bj < 2; ++bj)
; #pragma unroll
;                     for (int n = 0; n < 2; ++n) v[bj][n] = acc[ai][bj][m][n] * rs;
;                 if (!GATES && type <= 1) { float ss = 0.f;
; #pragma unroll
;                     for (int bj = 0; bj < 2; ++bj)
; #pragma unroll
;                         for (int n = 0; n < 2; ++n) ss += (v[bj][n][0] * v[bj][n][0] + v[bj][n][1] * v[bj][n][1]) + (v[bj][n][2] * v[bj][n][2] + v[bj][n][3] * v[bj][n][3]);
;                     ss += swz_f<16>(ss); ss = sum_x32(ss);
;                     const float r = __builtin_amdgcn_rsqf(ss * (1.f / 64.f) + EPS) * gsc;
; #pragma unroll
;                     for (int bj = 0; bj < 2; ++bj)
; #pragma unroll
;                         for (int n = 0; n < 2; ++n) v[bj][n] = v[bj][n] * r * *(const f32x4*)(gp + 32 * bj + 4 * n);
;                 } else if (type == 3) {
; #pragma unroll
;                     for (int bj = 0; bj < 2; ++bj)
; #pragma unroll
;                         for (int n = 0; n < 2; ++n)
; #pragma unroll
;                             for (int e = 0; e < 4; ++e) v[bj][n][e] = fast_gelu_tanh(v[bj][n][e]);
;                 } else if (type == 4) {
; #pragma unroll
;                     for (int bj = 0; bj < 2; ++bj)
; #pragma unroll
;                         for (int n = 0; n < 2; ++n)
.LBB0_355:
	s_cmp_lt_u32 s17, 14
	s_cselect_b32 s2, 3, 4
	s_cmp_gt_u32 s17, 9
	s_cselect_b32 s2, s2, 2
	s_cmp_lg_u32 s17, 4
	s_cselect_b32 s16, s2, 1
	s_cmp_lt_i32 s17, 4
	s_cselect_b64 s[2:3], -1, 0
	s_and_b64 s[6:7], s[2:3], exec
	s_cselect_b32 s6, s8, s10
	s_cselect_b32 s7, s9, s11
	s_add_u32 s6, s6, s22
	v_mov_b32_e32 v179, v169
	v_mov_b32_e32 v128, v168
	s_addc_u32 s7, s7, s23
	s_lshl_b32 s25, s25, 8
	s_add_i32 s25, s25, s48
	v_add_u32_e32 v142, s25, v128
	v_lshlrev_b32_e32 v128, 2, v179
	v_ashrrev_i32_e32 v129, 31, v128
	v_ashrrev_i32_e32 v143, 31, v142
	v_lshl_add_u64 v[146:147], v[128:129], 2, s[62:63]
	v_lshlrev_b64 v[128:129], 6, v[142:143]
	v_lshl_add_u64 v[128:129], v[146:147], 0, v[128:129]
	v_add_co_u32_e32 v212, vcc, 0x2000, v128
	global_load_dwordx4 v[180:183], v[128:129], off
	global_load_dwordx4 v[184:187], v[128:129], off offset:1024
	v_addc_co_u32_e32 v213, vcc, 0, v129, vcc
	global_load_dwordx4 v[188:191], v[128:129], off offset:2048
	global_load_dwordx4 v[192:195], v[128:129], off offset:3072
	global_load_dwordx4 v[196:199], v[212:213], off
	global_load_dwordx4 v[200:203], v[212:213], off offset:1024
	global_load_dwordx4 v[204:207], v[212:213], off offset:2048
	global_load_dwordx4 v[208:211], v[212:213], off offset:3072
	v_add_u32_e32 v140, 16, v142
	v_add_u32_e32 v138, 32, v142
	v_add_u32_e32 v136, 48, v142
	v_add_u32_e32 v134, 0x80, v142
	v_add_u32_e32 v132, 0x90, v142
	v_add_u32_e32 v130, 0xa0, v142
	s_cmp_gt_i32 s17, 4
	s_cselect_b64 s[28:29], -1, 0
	s_mov_b64 s[30:31], -1
	s_and_b64 vcc, exec, s[28:29]
	s_waitcnt vmcnt(0)
	v_add_f32_e32 v180, v181, v180
	v_add_f32_e32 v182, v182, v183
	v_add_f32_e32 v184, v184, v185
	v_add_f32_e32 v186, v186, v187
	v_add_f32_e32 v188, v188, v189
	v_add_f32_e32 v190, v190, v191
	v_add_f32_e32 v192, v192, v193
	v_add_f32_e32 v194, v194, v195
	v_add_f32_e32 v196, v196, v197
	v_add_f32_e32 v198, v198, v199
	v_add_f32_e32 v200, v200, v201
	v_add_f32_e32 v202, v202, v203
	v_add_f32_e32 v204, v204, v205
	v_add_f32_e32 v206, v206, v207
	v_add_f32_e32 v208, v208, v209
	v_add_f32_e32 v210, v210, v211
	v_add_f32_e32 v180, v180, v182
	v_add_f32_e32 v184, v184, v186
	v_add_f32_e32 v188, v188, v190
	v_add_f32_e32 v192, v192, v194
	v_add_f32_e32 v196, v196, v198
	v_add_f32_e32 v200, v200, v202
	v_add_f32_e32 v204, v204, v206
	v_add_f32_e32 v208, v208, v210
	ds_swizzle_b32 v181, v180 offset:swizzle(SWAP,16)
	ds_swizzle_b32 v185, v184 offset:swizzle(SWAP,16)
	ds_swizzle_b32 v189, v188 offset:swizzle(SWAP,16)
	ds_swizzle_b32 v193, v192 offset:swizzle(SWAP,16)
	ds_swizzle_b32 v197, v196 offset:swizzle(SWAP,16)
	ds_swizzle_b32 v201, v200 offset:swizzle(SWAP,16)
	ds_swizzle_b32 v205, v204 offset:swizzle(SWAP,16)
	ds_swizzle_b32 v209, v208 offset:swizzle(SWAP,16)
	s_waitcnt lgkmcnt(0)
	v_add_f32_e32 v128, v180, v181
	v_add_f32_e32 v143, v184, v185
	v_add_f32_e32 v176, v188, v189
	v_add_f32_e32 v174, v192, v193
	v_add_f32_e32 v172, v196, v197
	v_add_f32_e32 v139, v200, v201
	v_add_f32_e32 v135, v204, v205
	v_add_f32_e32 v131, v208, v209
	v_mov_b32_e32 v129, v128
	v_mov_b32_e32 v178, v143
	v_mov_b32_e32 v177, v176
	v_mov_b32_e32 v175, v174
	v_mov_b32_e32 v173, v172
	v_mov_b32_e32 v141, v139
	v_mov_b32_e32 v137, v135
	v_mov_b32_e32 v133, v131
	s_nop 1
	v_permlane32_swap_b32_e32 v128, v129
	v_permlane32_swap_b32_e32 v143, v178
	v_permlane32_swap_b32_e32 v176, v177
	v_permlane32_swap_b32_e32 v174, v175
	v_permlane32_swap_b32_e32 v172, v173
	v_permlane32_swap_b32_e32 v139, v141
	v_permlane32_swap_b32_e32 v135, v137
	v_permlane32_swap_b32_e32 v131, v133
	v_add_f32_e32 v128, v128, v129
	v_fmamk_f32 v128, v128, 0x3a800000, v230
	v_rsq_f32_e32 v144, v128
	v_add_u32_e32 v128, 0xb0, v142
	v_pk_mul_f32 v[152:153], v[126:127], v[144:145] op_sel_hi:[1,0]
	v_pk_mul_f32 v[154:155], v[124:125], v[144:145] op_sel_hi:[1,0]
	v_pk_mul_f32 v[122:123], v[122:123], v[144:145] op_sel_hi:[1,0]
	v_pk_mul_f32 v[124:125], v[120:121], v[144:145] op_sel_hi:[1,0]
	v_pk_mul_f32 v[120:121], v[118:119], v[144:145] op_sel_hi:[1,0]
	v_pk_mul_f32 v[126:127], v[116:117], v[144:145] op_sel_hi:[1,0]
	v_pk_mul_f32 v[116:117], v[114:115], v[144:145] op_sel_hi:[1,0]
	v_pk_mul_f32 v[118:119], v[112:113], v[144:145] op_sel_hi:[1,0]
	s_cbranch_vccz .LBB0_362
	s_cmp_gt_i32 s16, 3
	s_cbranch_scc0 .LBB0_358
	v_mul_f32_e32 v112, 0xbfb8aa3b, v154
	v_mul_f32_e32 v113, 0xbfb8aa3b, v155
	v_exp_f32_e32 v112, v112
	v_exp_f32_e32 v113, v113
	v_mul_f32_e32 v114, 0xbfb8aa3b, v152
	v_exp_f32_e32 v114, v114
	v_add_f32_e32 v112, 1.0, v112
	v_add_f32_e32 v113, 1.0, v113
	v_rcp_f32_e32 v112, v112
	v_rcp_f32_e32 v113, v113
	v_mul_f32_e32 v115, 0xbfb8aa3b, v125
	v_exp_f32_e32 v115, v115
	v_max_f32_e32 v146, 0x33800000, v112
	v_max_f32_e32 v147, 0x33800000, v113
	v_add_f32_e32 v112, 1.0, v114
	v_mul_f32_e32 v113, 0xbfb8aa3b, v153
	v_mul_f32_e32 v114, 0xbfb8aa3b, v124
	v_exp_f32_e32 v113, v113
	v_exp_f32_e32 v114, v114
	v_rcp_f32_e32 v112, v112
	s_mov_b64 s[30:31], 0
	v_add_f32_e32 v113, 1.0, v113
	v_add_f32_e32 v114, 1.0, v114
	v_rcp_f32_e32 v113, v113
	v_rcp_f32_e32 v114, v114
	v_max_f32_e32 v144, 0x33800000, v112
	v_add_f32_e32 v112, 1.0, v115
	v_max_f32_e32 v145, 0x33800000, v113
	v_max_f32_e32 v148, 0x33800000, v114
	v_mul_f32_e32 v113, 0xbfb8aa3b, v122
	v_mul_f32_e32 v114, 0xbfb8aa3b, v123
	v_exp_f32_e32 v113, v113
	v_exp_f32_e32 v114, v114
	v_mul_f32_e32 v115, 0xbfb8aa3b, v126
	v_rcp_f32_e32 v112, v112
	v_add_f32_e32 v113, 1.0, v113
	v_add_f32_e32 v114, 1.0, v114
	v_rcp_f32_e32 v113, v113
	v_rcp_f32_e32 v114, v114
	v_exp_f32_e32 v115, v115
	v_max_f32_e32 v149, 0x33800000, v112
	v_max_f32_e32 v150, 0x33800000, v113
	v_max_f32_e32 v151, 0x33800000, v114
	v_mul_f32_e32 v113, 0xbfb8aa3b, v127
	v_mul_f32_e32 v114, 0xbfb8aa3b, v120
	v_exp_f32_e32 v113, v113
	v_exp_f32_e32 v114, v114
	v_add_f32_e32 v112, 1.0, v115
	v_mul_f32_e32 v115, 0xbfb8aa3b, v121
	v_add_f32_e32 v113, 1.0, v113
	v_add_f32_e32 v114, 1.0, v114
	v_rcp_f32_e32 v112, v112
	v_rcp_f32_e32 v113, v113
	v_rcp_f32_e32 v114, v114
	v_exp_f32_e32 v115, v115
	v_max_f32_e32 v158, 0x33800000, v112
	v_max_f32_e32 v159, 0x33800000, v113
	v_max_f32_e32 v156, 0x33800000, v114
	v_add_f32_e32 v112, 1.0, v115
	v_mul_f32_e32 v113, 0xbfb8aa3b, v118
	v_mul_f32_e32 v114, 0xbfb8aa3b, v119
	v_rcp_f32_e32 v112, v112
	v_exp_f32_e32 v113, v113
	v_exp_f32_e32 v114, v114
	v_mul_f32_e32 v115, 0xbfb8aa3b, v117
	v_max_f32_e32 v157, 0x33800000, v112
	v_add_f32_e32 v112, 1.0, v113
	v_add_f32_e32 v113, 1.0, v114
	v_mul_f32_e32 v114, 0xbfb8aa3b, v116
	v_exp_f32_e32 v114, v114
	v_exp_f32_e32 v115, v115
	v_rcp_f32_e32 v112, v112
	v_rcp_f32_e32 v113, v113
	v_add_f32_e32 v114, 1.0, v114
	v_add_f32_e32 v115, 1.0, v115
	v_rcp_f32_e32 v114, v114
	v_rcp_f32_e32 v115, v115
	v_max_f32_e32 v162, 0x33800000, v112
	v_max_f32_e32 v163, 0x33800000, v113
	v_max_f32_e32 v160, 0x33800000, v114
	v_max_f32_e32 v161, 0x33800000, v115

; __device__ __forceinline__ float opaque_f(float x) { asm volatile("" : "+v"(x)); return x; }
; template <int MASK> __device__ __forceinline__ float swz_f(float v) { return __builtin_bit_cast(float, __builtin_amdgcn_ds_swizzle(__builtin_bit_cast(int, v), (MASK << 10) | 0x1f)); }
; __device__ __forceinline__ float sum_x32(float v) { const unsigned u = __builtin_bit_cast(unsigned, v); auto rr = __builtin_amdgcn_permlane32_swap(u, u, false, false); return __builtin_bit_cast(float, (unsigned)rr[0]) + __builtin_bit_cast(float, (unsigned)rr[1]); }
; __device__ __forceinline__ float rstd_q(const float* ssq, int row, int fq) {
;     const f32x4 p = *(const f32x4*)(ssq + 16 * (size_t)row + 4 * fq); float s = (p.x + p.y) + (p.z + p.w); s += swz_f<16>(s); s = sum_x32(s);
;     return __builtin_amdgcn_rsqf(s * (1.f / 1024.f) + EPS);
;     __device__ __forceinline__ void operator()(const f32x4 (&acc)[2][2][4][2], const Unit& u, int wr, int wc, int fr, int fq, const float* pre = nullptr) const {
;         float rs8[2][4], gw8[2][4];
; #pragma unroll
;         for (int ai = 0; ai < 2; ++ai)
; #pragma unroll
;             for (int m = 0; m < 4; ++m) { const int row = EPI_ROWS(ai, m); float rs, gw = 1.f;
;                 if (MOE) { rs = (MOE_FP8 ? opaque_f(1.f / W13_SCALE) : srs[row]); gw = (HAS_PRE ? pre[ai * 4 + m] : sgw[row]) * (MOE_FP8 ? G8_SCALE : 1.f); } else { rs = rstd_q(ssq, row, fq) * ascale; if (f8) gw = G8_SCALE; }
;                 rs8[ai][m] = rs; gw8[ai][m] = gw; }
.LBB0_1631:
	v_mov_b32_e32 v163, v157
	v_mov_b32_e32 v128, v153
	s_lshl_b32 s6, s58, 8
	s_add_i32 s6, s6, s45
	v_add_u32_e32 v158, s6, v128
	v_lshlrev_b32_e32 v128, 2, v163
	v_ashrrev_i32_e32 v129, 31, v128
	v_ashrrev_i32_e32 v159, 31, v158
	v_lshl_add_u64 v[128:129], v[128:129], 2, s[10:11]
	v_lshlrev_b64 v[130:131], 6, v[158:159]
	v_lshl_add_u64 v[130:131], v[128:129], 0, v[130:131]
	v_add_co_u32_e32 v208, vcc, 0x2000, v130
	global_load_dwordx4 v[180:183], v[130:131], off offset:1024
	global_load_dwordx4 v[184:187], v[130:131], off offset:2048
	v_addc_co_u32_e32 v209, vcc, 0, v131, vcc
	global_load_dwordx4 v[188:191], v[130:131], off offset:3072
	global_load_dwordx4 v[192:195], v[208:209], off
	global_load_dwordx4 v[196:199], v[208:209], off offset:1024
	global_load_dwordx4 v[200:203], v[208:209], off offset:2048
	global_load_dwordx4 v[204:207], v[208:209], off offset:3072
	global_load_dwordx4 v[130:133], v[130:131], off
	v_add_u32_e32 v154, 16, v158
	v_ashrrev_i32_e32 v155, 31, v154
	v_add_u32_e32 v150, 32, v158
	v_ashrrev_i32_e32 v151, 31, v150
	v_add_u32_e32 v146, 48, v158
	v_ashrrev_i32_e32 v147, 31, v146
	v_add_u32_e32 v142, 0x80, v158
	v_ashrrev_i32_e32 v143, 31, v142
	v_add_u32_e32 v138, 0x90, v158
	v_ashrrev_i32_e32 v139, 31, v138
	s_movk_i32 s58, 0x1c00
	s_andn2_b64 vcc, exec, s[18:19]
	s_waitcnt vmcnt(0)
	v_mov_b32_e32 v134, v131
	v_mov_b32_e32 v135, v132
	v_mov_b32_e32 v131, v133
	v_pk_add_f32 v[130:131], v[134:135], v[130:131]
	s_nop 0
	v_add_f32_e32 v130, v130, v131
	ds_swizzle_b32 v131, v130 offset:swizzle(SWAP,16)
	s_waitcnt lgkmcnt(0)
	v_add_f32_e32 v130, v130, v131
	v_mov_b32_e32 v131, v130
	s_nop 1
	v_permlane32_swap_b32_e32 v130, v131
	v_add_f32_e32 v130, v130, v131
	v_fmamk_f32 v130, v130, 0x3a800000, v230
	v_rsq_f32_e32 v160, v130
	s_nop 1
	s_waitcnt vmcnt(0)
	v_mov_b32_e32 v130, v180
	v_mov_b32_e32 v131, v181
	v_mov_b32_e32 v132, v182
	v_mov_b32_e32 v133, v183
	v_mov_b32_e32 v134, v131
	v_mov_b32_e32 v135, v132
	v_mov_b32_e32 v131, v133
	v_pk_add_f32 v[130:131], v[134:135], v[130:131]
	s_nop 0
	v_add_f32_e32 v130, v130, v131
	ds_swizzle_b32 v131, v130 offset:swizzle(SWAP,16)
	s_waitcnt lgkmcnt(0)
	v_add_f32_e32 v130, v130, v131
	v_mov_b32_e32 v131, v130
	s_nop 1
	v_permlane32_swap_b32_e32 v130, v131
	v_add_f32_e32 v130, v130, v131
	v_fmamk_f32 v130, v130, 0x3a800000, v230
	v_rsq_f32_e32 v156, v130
	s_nop 1
	s_waitcnt vmcnt(0)
	v_mov_b32_e32 v130, v184
	v_mov_b32_e32 v131, v185
	v_mov_b32_e32 v132, v186
	v_mov_b32_e32 v133, v187
	v_mov_b32_e32 v134, v131
	v_mov_b32_e32 v135, v132
	v_mov_b32_e32 v131, v133
	v_pk_add_f32 v[130:131], v[134:135], v[130:131]
	s_nop 0
	v_add_f32_e32 v130, v130, v131
	ds_swizzle_b32 v131, v130 offset:swizzle(SWAP,16)
	s_waitcnt lgkmcnt(0)
	v_add_f32_e32 v130, v130, v131
	v_mov_b32_e32 v131, v130
	s_nop 1
	v_permlane32_swap_b32_e32 v130, v131
	v_add_f32_e32 v130, v130, v131
	v_fmamk_f32 v130, v130, 0x3a800000, v230
	v_rsq_f32_e32 v152, v130
	s_nop 1
	s_waitcnt vmcnt(0)
	v_mov_b32_e32 v130, v188
	v_mov_b32_e32 v131, v189
	v_mov_b32_e32 v132, v190
	v_mov_b32_e32 v133, v191
	v_mov_b32_e32 v134, v131
	v_mov_b32_e32 v135, v132
	v_mov_b32_e32 v131, v133
	v_pk_add_f32 v[130:131], v[134:135], v[130:131]
	s_nop 0
	v_add_f32_e32 v130, v130, v131
	ds_swizzle_b32 v131, v130 offset:swizzle(SWAP,16)
	s_waitcnt lgkmcnt(0)
	v_add_f32_e32 v130, v130, v131
	v_mov_b32_e32 v131, v130
	s_nop 1
	v_permlane32_swap_b32_e32 v130, v131
	v_add_f32_e32 v130, v130, v131
	v_fmamk_f32 v130, v130, 0x3a800000, v230
	v_rsq_f32_e32 v148, v130
	s_nop 1
	s_waitcnt vmcnt(0)
	v_mov_b32_e32 v130, v192
	v_mov_b32_e32 v131, v193
	v_mov_b32_e32 v132, v194
	v_mov_b32_e32 v133, v195
	v_mov_b32_e32 v134, v131
	v_mov_b32_e32 v135, v132
	v_mov_b32_e32 v131, v133
	v_pk_add_f32 v[130:131], v[134:135], v[130:131]
	s_nop 0
	v_add_f32_e32 v130, v130, v131
	ds_swizzle_b32 v131, v130 offset:swizzle(SWAP,16)
	s_waitcnt lgkmcnt(0)
	v_add_f32_e32 v130, v130, v131
	v_mov_b32_e32 v131, v130
	s_nop 1
	v_permlane32_swap_b32_e32 v130, v131
	v_add_f32_e32 v130, v130, v131
	v_fmamk_f32 v130, v130, 0x3a800000, v230
	v_rsq_f32_e32 v144, v130
	s_nop 1
	s_waitcnt vmcnt(0)
	v_mov_b32_e32 v130, v196
	v_mov_b32_e32 v131, v197
	v_mov_b32_e32 v132, v198
	v_mov_b32_e32 v133, v199
	v_mov_b32_e32 v134, v131
	v_mov_b32_e32 v135, v132
	v_mov_b32_e32 v131, v133
	v_pk_add_f32 v[130:131], v[134:135], v[130:131]
	v_add_u32_e32 v134, 0xa0, v158
	v_add_f32_e32 v130, v130, v131
	ds_swizzle_b32 v131, v130 offset:swizzle(SWAP,16)
	v_ashrrev_i32_e32 v135, 31, v134
	s_waitcnt lgkmcnt(0)
	v_add_f32_e32 v130, v130, v131
	v_mov_b32_e32 v131, v130
	s_nop 1
	v_permlane32_swap_b32_e32 v130, v131
	v_add_f32_e32 v130, v130, v131
	v_fmamk_f32 v130, v130, 0x3a800000, v230
	v_rsq_f32_e32 v140, v130
	s_nop 1
	s_waitcnt vmcnt(0)
	v_mov_b32_e32 v130, v200
	v_mov_b32_e32 v131, v201
	v_mov_b32_e32 v132, v202
	v_mov_b32_e32 v133, v203
	v_mov_b32_e32 v164, v131
	v_mov_b32_e32 v165, v132
	v_mov_b32_e32 v131, v133
	v_pk_add_f32 v[130:131], v[164:165], v[130:131]
	v_add_u32_e32 v132, 0xb0, v158
	v_add_f32_e32 v130, v130, v131
	ds_swizzle_b32 v131, v130 offset:swizzle(SWAP,16)
	v_ashrrev_i32_e32 v133, 31, v132
	s_waitcnt lgkmcnt(0)
	v_add_f32_e32 v130, v130, v131
	v_mov_b32_e32 v131, v130
	s_nop 1
	v_permlane32_swap_b32_e32 v130, v131
	v_add_f32_e32 v130, v130, v131
	v_fmamk_f32 v130, v130, 0x3a800000, v230
	v_rsq_f32_e32 v136, v130
	s_nop 1
	s_waitcnt vmcnt(0)
; __device__ __forceinline__ float opaque_f(float x) { asm volatile("" : "+v"(x)); return x; }
; __device__ __forceinline__ float fast_sigmoid(float x) { return __builtin_amdgcn_rcpf(1.f + __builtin_amdgcn_exp2f(-LOG2E * x)); }
; __device__ __forceinline__ u32x4 pack8(const f32x4 a, const f32x4 b) { u32x4 w; w.x = cvt_pk_bf16(a[0], a[1]); w.y = cvt_pk_bf16(a[2], a[3]); w.z = cvt_pk_bf16(b[0], b[1]); w.w = cvt_pk_bf16(b[2], b[3]); return w; }
;     __device__ __forceinline__ void operator()(const f32x4 (&acc)[2][2][4][2], const Unit& u, int wr, int wc, int fr, int fq, const float* pre = nullptr) const {
;     ...
;             for (int m = 0; m < 4; ++m) { const int row = EPI_ROWS(ai, m); float rs, gw = 1.f;
;                 if (MOE) { rs = (MOE_FP8 ? opaque_f(1.f / W13_SCALE) : srs[row]); gw = (HAS_PRE ? pre[ai * 4 + m] : sgw[row]) * (MOE_FP8 ? G8_SCALE : 1.f); } else { rs = rstd_q(ssq, row, fq) * ascale; if (f8) gw = G8_SCALE; }
;                 rs8[ai][m] = rs; gw8[ai][m] = gw; }
; #pragma unroll
;         for (int ai = 0; ai < 2; ++ai)
; #pragma unroll
;             for (int m = 0; m < 4; ++m) { const int row = EPI_ROWS(ai, m); const float rs = rs8[ai][m], gw = gw8[ai][m];
;                 const float rs2 = rs * gw; f32x4 o[2];
; #pragma unroll
;                 for (int bj = 0; bj < 2; ++bj)
; #pragma unroll
;                     for (int e = 0; e < 4; ++e) { const float a = acc[ai][bj][m][0][e] * rs, b = acc[ai][bj][m][1][e] * rs2; o[bj][e] = a * fast_sigmoid(a) * b; }
;                 if ((MOE && MOE_FP8) || (!MOE && f8)) { u32x2 w; w.x = pk4_fp8(o[0][0], o[0][1], o[0][2], o[0][3]); w.y = pk4_fp8(o[1][0], o[1][1], o[1][2], o[1][3]);
;                     *(u32x2*)((unsigned char*)G + (size_t)row * DFF + u.pn * HALF + wc * 32 + 8 * fq) = w; }
;                 else *(u32x4*)(G + (size_t)row * DFF + u.pn * HALF + wc * 32 + 8 * fq) = pack8(o[0], o[1]); }
	v_mov_b32_e32 v128, v204
	v_mov_b32_e32 v129, v205
	v_mov_b32_e32 v130, v206
	v_mov_b32_e32 v131, v207
	v_mov_b32_e32 v164, v129
	v_mov_b32_e32 v165, v130
	v_mov_b32_e32 v129, v131
	v_pk_add_f32 v[128:129], v[164:165], v[128:129]
	v_mov_b32_e32 v164, v124
	v_mov_b32_e32 v165, v120
	v_pk_mul_f32 v[164:165], v[164:165], v[160:161] op_sel_hi:[1,0]
	v_lshlrev_b32_e32 v130, 3, v163
	v_mul_f32_e32 v120, 0xbfb8aa3b, v165
	v_exp_f32_e32 v120, v120
	v_ashrrev_i32_e32 v131, 31, v130
	v_add_f32_e32 v128, v128, v129
	ds_swizzle_b32 v129, v128 offset:swizzle(SWAP,16)
	v_add_f32_e32 v120, 1.0, v120
	v_rcp_f32_e32 v120, v120
	s_waitcnt lgkmcnt(0)
	v_add_f32_e32 v128, v128, v129
	v_mul_f32_e32 v120, v165, v120
	v_mul_f32_e32 v124, v164, v120
	v_mov_b32_e32 v120, v125
	v_pk_mul_f32 v[120:121], v[120:121], v[160:161] op_sel_hi:[1,0]
	v_mov_b32_e32 v129, v128
	v_mul_f32_e32 v125, 0xbfb8aa3b, v121
	v_exp_f32_e32 v125, v125
	v_permlane32_swap_b32_e32 v128, v129
	v_add_f32_e32 v128, v128, v129
	v_add_f32_e32 v125, 1.0, v125
	v_rcp_f32_e32 v125, v125
	v_fmamk_f32 v128, v128, 0x3a800000, v230
	v_rsq_f32_e32 v128, v128
	v_mul_f32_e32 v121, v121, v125
	v_mul_f32_e32 v125, v120, v121
	v_mov_b32_e32 v120, v126
	v_mov_b32_e32 v121, v122
	v_pk_mul_f32 v[120:121], v[120:121], v[160:161] op_sel_hi:[1,0]
	s_nop 0
	v_mul_f32_e32 v122, 0xbfb8aa3b, v121
	v_exp_f32_e32 v122, v122
	s_nop 0
	v_add_f32_e32 v122, 1.0, v122
	v_rcp_f32_e32 v122, v122
	s_nop 0
	v_mul_f32_e32 v121, v121, v122
	v_mov_b32_e32 v122, v127
	v_mul_f32_e32 v126, v120, v121
	v_pk_mul_f32 v[120:121], v[122:123], v[160:161] op_sel_hi:[1,0]
	s_nop 0
	v_mul_f32_e32 v122, 0xbfb8aa3b, v121
	v_exp_f32_e32 v122, v122
	s_nop 0
	v_add_f32_e32 v122, 1.0, v122
	v_rcp_f32_e32 v122, v122
	s_nop 0
	v_mul_f32_e32 v121, v121, v122
	v_mul_f32_e32 v122, v120, v121
	v_mov_b32_e32 v120, v116
	v_mov_b32_e32 v121, v112
	v_pk_mul_f32 v[120:121], v[120:121], v[160:161] op_sel_hi:[1,0]
	s_nop 0
	v_mul_f32_e32 v112, 0xbfb8aa3b, v121
	v_exp_f32_e32 v112, v112
	s_nop 0
	v_add_f32_e32 v112, 1.0, v112
	v_rcp_f32_e32 v112, v112
	s_nop 0
	v_mul_f32_e32 v112, v121, v112
	v_mul_f32_e32 v120, v120, v112
	v_mov_b32_e32 v112, v117
	v_pk_mul_f32 v[112:113], v[112:113], v[160:161] op_sel_hi:[1,0]
	s_nop 0
	v_mul_f32_e32 v116, 0xbfb8aa3b, v113
	v_exp_f32_e32 v116, v116
	s_nop 0
	v_add_f32_e32 v116, 1.0, v116
	v_rcp_f32_e32 v116, v116
	s_nop 0
	v_mul_f32_e32 v113, v113, v116
	v_mul_f32_e32 v121, v112, v113
	v_mov_b32_e32 v112, v118
	v_mov_b32_e32 v113, v114
	v_pk_mul_f32 v[112:113], v[112:113], v[160:161] op_sel_hi:[1,0]
	v_cvt_pk_bf16_f32 v116, v124, v125
	v_cvt_pk_bf16_f32 v117, v126, v122
	v_cvt_pk_bf16_f32 v118, v120, v121
	s_nop 0
	v_mul_f32_e32 v114, 0xbfb8aa3b, v113
	v_exp_f32_e32 v114, v114
	s_nop 0
	v_add_f32_e32 v114, 1.0, v114
	v_rcp_f32_e32 v114, v114
	s_nop 0
	v_mul_f32_e32 v113, v113, v114
	v_mov_b32_e32 v114, v119
	v_mul_f32_e32 v123, v112, v113
	v_pk_mul_f32 v[112:113], v[114:115], v[160:161] op_sel_hi:[1,0]
	s_nop 0
	v_mul_f32_e32 v114, 0xbfb8aa3b, v113
	v_exp_f32_e32 v114, v114
	s_nop 0
	v_add_f32_e32 v114, 1.0, v114
	v_rcp_f32_e32 v114, v114
	s_nop 0
	v_mul_f32_e32 v113, v113, v114
	v_mul_f32_e32 v112, v112, v113
	v_cvt_pk_bf16_f32 v119, v123, v112
	v_mov_b64_e32 v[112:113], s[8:9]
	v_mad_i64_i32 v[114:115], s[6:7], v158, s58, v[112:113]
	s_lshl_b32 s6, s17, 7
	s_ashr_i32 s7, s6, 31
	s_lshl_b64 s[6:7], s[6:7], 1
	v_lshl_add_u64 v[114:115], v[114:115], 0, s[6:7]
	s_mov_b32 s17, s40
	v_lshl_add_u64 v[120:121], v[114:115], 0, s[16:17]
	v_lshlrev_b64 v[114:115], 1, v[130:131]
	v_lshl_add_u64 v[120:121], v[120:121], 0, v[114:115]
	global_store_dwordx4 v[120:121], v[116:119], off
	s_nop 1
	v_mov_b32_e32 v116, v108
	v_mov_b32_e32 v117, v104
	v_pk_mul_f32 v[116:117], v[116:117], v[156:157] op_sel_hi:[1,0]
	s_nop 0
	v_mul_f32_e32 v104, 0xbfb8aa3b, v117
	v_exp_f32_e32 v104, v104
	s_nop 0
	v_add_f32_e32 v104, 1.0, v104
	v_rcp_f32_e32 v104, v104
	s_nop 0
	v_mul_f32_e32 v104, v117, v104
	v_mul_f32_e32 v108, v116, v104
	v_mov_b32_e32 v104, v109
	v_pk_mul_f32 v[104:105], v[104:105], v[156:157] op_sel_hi:[1,0]
	s_nop 0
	v_mul_f32_e32 v109, 0xbfb8aa3b, v105
	v_exp_f32_e32 v109, v109
	s_nop 0
	v_add_f32_e32 v109, 1.0, v109
	v_rcp_f32_e32 v109, v109
	s_nop 0
	v_mul_f32_e32 v105, v105, v109
	v_mul_f32_e32 v109, v104, v105
	v_mov_b32_e32 v104, v110
	v_mov_b32_e32 v105, v106
	v_pk_mul_f32 v[104:105], v[104:105], v[156:157] op_sel_hi:[1,0]
	s_nop 0
	v_mul_f32_e32 v106, 0xbfb8aa3b, v105
	v_exp_f32_e32 v106, v106
	s_nop 0
	v_add_f32_e32 v106, 1.0, v106
	v_rcp_f32_e32 v106, v106
	s_nop 0
	v_mul_f32_e32 v105, v105, v106
	v_mov_b32_e32 v106, v111
	v_mul_f32_e32 v110, v104, v105
	v_pk_mul_f32 v[104:105], v[106:107], v[156:157] op_sel_hi:[1,0]
	s_nop 0
	v_mul_f32_e32 v106, 0xbfb8aa3b, v105
	v_exp_f32_e32 v106, v106
	s_nop 0
	v_add_f32_e32 v106, 1.0, v106
	v_rcp_f32_e32 v106, v106
	s_nop 0
	v_mul_f32_e32 v105, v105, v106
	v_mul_f32_e32 v106, v104, v105
	v_mov_b32_e32 v104, v100
	v_mov_b32_e32 v105, v96
	v_pk_mul_f32 v[104:105], v[104:105], v[156:157] op_sel_hi:[1,0]
	s_nop 0
	v_mul_f32_e32 v96, 0xbfb8aa3b, v105
	v_exp_f32_e32 v96, v96
	s_nop 0
	v_add_f32_e32 v96, 1.0, v96
	v_rcp_f32_e32 v96, v96
	s_nop 0
	v_mul_f32_e32 v96, v105, v96
	v_mul_f32_e32 v100, v104, v96
	v_mov_b32_e32 v96, v101
	v_pk_mul_f32 v[96:97], v[96:97], v[156:157] op_sel_hi:[1,0]
	s_nop 0
	v_mul_f32_e32 v101, 0xbfb8aa3b, v97
	v_exp_f32_e32 v101, v101
	s_nop 0
	v_add_f32_e32 v101, 1.0, v101
	v_rcp_f32_e32 v101, v101
	s_nop 0
	v_mul_f32_e32 v97, v97, v101
	v_mul_f32_e32 v101, v96, v97
	v_mov_b32_e32 v96, v102
	v_mov_b32_e32 v97, v98
	v_pk_mul_f32 v[96:97], v[96:97], v[156:157] op_sel_hi:[1,0]
; __device__ __forceinline__ float fast_sigmoid(float x) { return __builtin_amdgcn_rcpf(1.f + __builtin_amdgcn_exp2f(-LOG2E * x)); }
; __device__ __forceinline__ u32x4 pack8(const f32x4 a, const f32x4 b) { u32x4 w; w.x = cvt_pk_bf16(a[0], a[1]); w.y = cvt_pk_bf16(a[2], a[3]); w.z = cvt_pk_bf16(b[0], b[1]); w.w = cvt_pk_bf16(b[2], b[3]); return w; }
;     __device__ __forceinline__ void operator()(const f32x4 (&acc)[2][2][4][2], const Unit& u, int wr, int wc, int fr, int fq, const float* pre = nullptr) const {
;     ...
;         for (int ai = 0; ai < 2; ++ai)
; #pragma unroll
;             for (int m = 0; m < 4; ++m) { const int row = EPI_ROWS(ai, m); const float rs = rs8[ai][m], gw = gw8[ai][m];
;                 const float rs2 = rs * gw; f32x4 o[2];
; #pragma unroll
;                 for (int bj = 0; bj < 2; ++bj)
; #pragma unroll
;                     for (int e = 0; e < 4; ++e) { const float a = acc[ai][bj][m][0][e] * rs, b = acc[ai][bj][m][1][e] * rs2; o[bj][e] = a * fast_sigmoid(a) * b; }
;                 if ((MOE && MOE_FP8) || (!MOE && f8)) { u32x2 w; w.x = pk4_fp8(o[0][0], o[0][1], o[0][2], o[0][3]); w.y = pk4_fp8(o[1][0], o[1][1], o[1][2], o[1][3]);
;                     *(u32x2*)((unsigned char*)G + (size_t)row * DFF + u.pn * HALF + wc * 32 + 8 * fq) = w; }
;                 else *(u32x4*)(G + (size_t)row * DFF + u.pn * HALF + wc * 32 + 8 * fq) = pack8(o[0], o[1]); }
	s_nop 0
	v_mul_f32_e32 v98, 0xbfb8aa3b, v97
	v_exp_f32_e32 v98, v98
	s_nop 0
	v_add_f32_e32 v98, 1.0, v98
	v_rcp_f32_e32 v98, v98
	s_nop 0
	v_mul_f32_e32 v97, v97, v98
	v_mov_b32_e32 v98, v103
	v_mul_f32_e32 v102, v96, v97
	v_pk_mul_f32 v[96:97], v[98:99], v[156:157] op_sel_hi:[1,0]
	s_nop 0
	v_mul_f32_e32 v98, 0xbfb8aa3b, v97
	v_exp_f32_e32 v98, v98
	s_nop 0
	v_add_f32_e32 v98, 1.0, v98
	v_rcp_f32_e32 v98, v98
	s_nop 0
	v_mul_f32_e32 v97, v97, v98
	v_mul_f32_e32 v99, v96, v97
	v_cvt_pk_bf16_f32 v96, v108, v109
	v_cvt_pk_bf16_f32 v97, v110, v106
	v_cvt_pk_bf16_f32 v98, v100, v101
	v_mad_i64_i32 v[100:101], s[54:55], v154, s58, v[112:113]
	v_lshl_add_u64 v[100:101], v[100:101], 0, s[6:7]
	v_lshl_add_u64 v[100:101], v[100:101], 0, s[16:17]
	v_lshl_add_u64 v[100:101], v[100:101], 0, v[114:115]
	v_cvt_pk_bf16_f32 v99, v102, v99
	global_store_dwordx4 v[100:101], v[96:99], off
	s_nop 1
	v_mov_b32_e32 v96, v92
	v_mov_b32_e32 v97, v88
	v_pk_mul_f32 v[96:97], v[96:97], v[152:153] op_sel_hi:[1,0]
	s_nop 0
	v_mul_f32_e32 v88, 0xbfb8aa3b, v97
	v_exp_f32_e32 v88, v88
	s_nop 0
	v_add_f32_e32 v88, 1.0, v88
	v_rcp_f32_e32 v88, v88
	s_nop 0
	v_mul_f32_e32 v88, v97, v88
	v_mul_f32_e32 v92, v96, v88
	v_mov_b32_e32 v88, v93
	v_pk_mul_f32 v[88:89], v[88:89], v[152:153] op_sel_hi:[1,0]
	s_nop 0
	v_mul_f32_e32 v93, 0xbfb8aa3b, v89
	v_exp_f32_e32 v93, v93
	s_nop 0
	v_add_f32_e32 v93, 1.0, v93
	v_rcp_f32_e32 v93, v93
	s_nop 0
	v_mul_f32_e32 v89, v89, v93
	v_mul_f32_e32 v93, v88, v89
	v_mov_b32_e32 v88, v94
	v_mov_b32_e32 v89, v90
	v_pk_mul_f32 v[88:89], v[88:89], v[152:153] op_sel_hi:[1,0]
	s_nop 0
	v_mul_f32_e32 v90, 0xbfb8aa3b, v89
	v_exp_f32_e32 v90, v90
	s_nop 0
	v_add_f32_e32 v90, 1.0, v90
	v_rcp_f32_e32 v90, v90
	s_nop 0
	v_mul_f32_e32 v89, v89, v90
	v_mov_b32_e32 v90, v95
	v_mul_f32_e32 v94, v88, v89
	v_pk_mul_f32 v[88:89], v[90:91], v[152:153] op_sel_hi:[1,0]
	s_nop 0
	v_mul_f32_e32 v90, 0xbfb8aa3b, v89
	v_exp_f32_e32 v90, v90
	s_nop 0
	v_add_f32_e32 v90, 1.0, v90
	v_rcp_f32_e32 v90, v90
	s_nop 0
	v_mul_f32_e32 v89, v89, v90
	v_mul_f32_e32 v90, v88, v89
	v_mov_b32_e32 v88, v84
	v_mov_b32_e32 v89, v80
	v_pk_mul_f32 v[88:89], v[88:89], v[152:153] op_sel_hi:[1,0]
	s_nop 0
	v_mul_f32_e32 v80, 0xbfb8aa3b, v89
	v_exp_f32_e32 v80, v80
	s_nop 0
	v_add_f32_e32 v80, 1.0, v80
	v_rcp_f32_e32 v80, v80
	s_nop 0
	v_mul_f32_e32 v80, v89, v80
	v_mul_f32_e32 v84, v88, v80
	v_mov_b32_e32 v80, v85
	v_pk_mul_f32 v[80:81], v[80:81], v[152:153] op_sel_hi:[1,0]
	s_nop 0
	v_mul_f32_e32 v85, 0xbfb8aa3b, v81
	v_exp_f32_e32 v85, v85
	s_nop 0
	v_add_f32_e32 v85, 1.0, v85
	v_rcp_f32_e32 v85, v85
	s_nop 0
	v_mul_f32_e32 v81, v81, v85
	v_mul_f32_e32 v85, v80, v81
	v_mov_b32_e32 v80, v86
	v_mov_b32_e32 v81, v82
	v_pk_mul_f32 v[80:81], v[80:81], v[152:153] op_sel_hi:[1,0]
	s_nop 0
	v_mul_f32_e32 v82, 0xbfb8aa3b, v81
	v_exp_f32_e32 v82, v82
	s_nop 0
	v_add_f32_e32 v82, 1.0, v82
	v_rcp_f32_e32 v82, v82
	s_nop 0
	v_mul_f32_e32 v81, v81, v82
	v_mov_b32_e32 v82, v87
	v_mul_f32_e32 v86, v80, v81
	v_pk_mul_f32 v[80:81], v[82:83], v[152:153] op_sel_hi:[1,0]
	s_nop 0
	v_mul_f32_e32 v82, 0xbfb8aa3b, v81
	v_exp_f32_e32 v82, v82
	s_nop 0
	v_add_f32_e32 v82, 1.0, v82
	v_rcp_f32_e32 v82, v82
	s_nop 0
	v_mul_f32_e32 v81, v81, v82
	v_mul_f32_e32 v83, v80, v81
	v_cvt_pk_bf16_f32 v80, v92, v93
	v_cvt_pk_bf16_f32 v81, v94, v90
	v_cvt_pk_bf16_f32 v82, v84, v85
	v_mad_i64_i32 v[84:85], s[54:55], v150, s58, v[112:113]
	v_lshl_add_u64 v[84:85], v[84:85], 0, s[6:7]
	v_lshl_add_u64 v[84:85], v[84:85], 0, s[16:17]
	v_lshl_add_u64 v[84:85], v[84:85], 0, v[114:115]
	v_cvt_pk_bf16_f32 v83, v86, v83
	global_store_dwordx4 v[84:85], v[80:83], off
	s_nop 1
	v_mov_b32_e32 v80, v76
	v_mov_b32_e32 v81, v72
	v_pk_mul_f32 v[80:81], v[80:81], v[148:149] op_sel_hi:[1,0]
	s_nop 0
	v_mul_f32_e32 v72, 0xbfb8aa3b, v81
	v_exp_f32_e32 v72, v72
	s_nop 0
	v_add_f32_e32 v72, 1.0, v72
	v_rcp_f32_e32 v72, v72
	s_nop 0
	v_mul_f32_e32 v72, v81, v72
	v_mul_f32_e32 v76, v80, v72
	v_mov_b32_e32 v72, v77
	v_pk_mul_f32 v[72:73], v[72:73], v[148:149] op_sel_hi:[1,0]
	s_nop 0
	v_mul_f32_e32 v77, 0xbfb8aa3b, v73
	v_exp_f32_e32 v77, v77
	s_nop 0
	v_add_f32_e32 v77, 1.0, v77
	v_rcp_f32_e32 v77, v77
	s_nop 0
	v_mul_f32_e32 v73, v73, v77
	v_mul_f32_e32 v77, v72, v73
	v_mov_b32_e32 v72, v78
	v_mov_b32_e32 v73, v74
	v_pk_mul_f32 v[72:73], v[72:73], v[148:149] op_sel_hi:[1,0]
	s_nop 0
	v_mul_f32_e32 v74, 0xbfb8aa3b, v73
	v_exp_f32_e32 v74, v74
	s_nop 0
	v_add_f32_e32 v74, 1.0, v74
	v_rcp_f32_e32 v74, v74
	s_nop 0
	v_mul_f32_e32 v73, v73, v74
	v_mov_b32_e32 v74, v79
	v_mul_f32_e32 v78, v72, v73
	v_pk_mul_f32 v[72:73], v[74:75], v[148:149] op_sel_hi:[1,0]
	s_nop 0
	v_mul_f32_e32 v74, 0xbfb8aa3b, v73
	v_exp_f32_e32 v74, v74
	s_nop 0
	v_add_f32_e32 v74, 1.0, v74
	v_rcp_f32_e32 v74, v74
	s_nop 0
	v_mul_f32_e32 v73, v73, v74
	v_mul_f32_e32 v74, v72, v73
	v_mov_b32_e32 v72, v68
	v_mov_b32_e32 v73, v64
	v_pk_mul_f32 v[72:73], v[72:73], v[148:149] op_sel_hi:[1,0]
	s_nop 0
	v_mul_f32_e32 v64, 0xbfb8aa3b, v73
	v_exp_f32_e32 v64, v64
	s_nop 0
	v_add_f32_e32 v64, 1.0, v64
	v_rcp_f32_e32 v64, v64
	s_nop 0
	v_mul_f32_e32 v64, v73, v64
	v_mul_f32_e32 v68, v72, v64
	v_mov_b32_e32 v64, v69
	v_pk_mul_f32 v[64:65], v[64:65], v[148:149] op_sel_hi:[1,0]
	s_nop 0
	v_mul_f32_e32 v69, 0xbfb8aa3b, v65
	v_exp_f32_e32 v69, v69
	s_nop 0
	v_add_f32_e32 v69, 1.0, v69
	v_rcp_f32_e32 v69, v69
	s_nop 0
	v_mul_f32_e32 v65, v65, v69
	v_mul_f32_e32 v69, v64, v65
	v_mov_b32_e32 v64, v70
	v_mov_b32_e32 v65, v66
	v_pk_mul_f32 v[64:65], v[64:65], v[148:149] op_sel_hi:[1,0]
	s_nop 0
	v_mul_f32_e32 v66, 0xbfb8aa3b, v65
	v_exp_f32_e32 v66, v66
	s_nop 0
	v_add_f32_e32 v66, 1.0, v66
; __device__ __forceinline__ float fast_sigmoid(float x) { return __builtin_amdgcn_rcpf(1.f + __builtin_amdgcn_exp2f(-LOG2E * x)); }
; __device__ __forceinline__ u32x4 pack8(const f32x4 a, const f32x4 b) { u32x4 w; w.x = cvt_pk_bf16(a[0], a[1]); w.y = cvt_pk_bf16(a[2], a[3]); w.z = cvt_pk_bf16(b[0], b[1]); w.w = cvt_pk_bf16(b[2], b[3]); return w; }
;     __device__ __forceinline__ void operator()(const f32x4 (&acc)[2][2][4][2], const Unit& u, int wr, int wc, int fr, int fq, const float* pre = nullptr) const {
;     ...
;         for (int ai = 0; ai < 2; ++ai)
; #pragma unroll
;             for (int m = 0; m < 4; ++m) { const int row = EPI_ROWS(ai, m); const float rs = rs8[ai][m], gw = gw8[ai][m];
;                 const float rs2 = rs * gw; f32x4 o[2];
; #pragma unroll
;                 for (int bj = 0; bj < 2; ++bj)
; #pragma unroll
;                     for (int e = 0; e < 4; ++e) { const float a = acc[ai][bj][m][0][e] * rs, b = acc[ai][bj][m][1][e] * rs2; o[bj][e] = a * fast_sigmoid(a) * b; }
;                 if ((MOE && MOE_FP8) || (!MOE && f8)) { u32x2 w; w.x = pk4_fp8(o[0][0], o[0][1], o[0][2], o[0][3]); w.y = pk4_fp8(o[1][0], o[1][1], o[1][2], o[1][3]);
;                     *(u32x2*)((unsigned char*)G + (size_t)row * DFF + u.pn * HALF + wc * 32 + 8 * fq) = w; }
;                 else *(u32x4*)(G + (size_t)row * DFF + u.pn * HALF + wc * 32 + 8 * fq) = pack8(o[0], o[1]); }
	v_rcp_f32_e32 v66, v66
	s_nop 0
	v_mul_f32_e32 v65, v65, v66
	v_mov_b32_e32 v66, v71
	v_mul_f32_e32 v70, v64, v65
	v_pk_mul_f32 v[64:65], v[66:67], v[148:149] op_sel_hi:[1,0]
	s_nop 0
	v_mul_f32_e32 v66, 0xbfb8aa3b, v65
	v_exp_f32_e32 v66, v66
	s_nop 0
	v_add_f32_e32 v66, 1.0, v66
	v_rcp_f32_e32 v66, v66
	s_nop 0
	v_mul_f32_e32 v65, v65, v66
	v_mul_f32_e32 v67, v64, v65
	v_cvt_pk_bf16_f32 v64, v76, v77
	v_cvt_pk_bf16_f32 v65, v78, v74
	v_cvt_pk_bf16_f32 v66, v68, v69
	v_mad_i64_i32 v[68:69], s[54:55], v146, s58, v[112:113]
	v_lshl_add_u64 v[68:69], v[68:69], 0, s[6:7]
	v_lshl_add_u64 v[68:69], v[68:69], 0, s[16:17]
	v_lshl_add_u64 v[68:69], v[68:69], 0, v[114:115]
	v_cvt_pk_bf16_f32 v67, v70, v67
	global_store_dwordx4 v[68:69], v[64:67], off
	s_nop 1
	v_mov_b32_e32 v64, v60
	v_mov_b32_e32 v65, v56
	v_pk_mul_f32 v[64:65], v[64:65], v[144:145] op_sel_hi:[1,0]
	s_nop 0
	v_mul_f32_e32 v56, 0xbfb8aa3b, v65
	v_exp_f32_e32 v56, v56
	s_nop 0
	v_add_f32_e32 v56, 1.0, v56
	v_rcp_f32_e32 v56, v56
	s_nop 0
	v_mul_f32_e32 v56, v65, v56
	v_mul_f32_e32 v60, v64, v56
	v_mov_b32_e32 v56, v61
	v_pk_mul_f32 v[56:57], v[56:57], v[144:145] op_sel_hi:[1,0]
	s_nop 0
	v_mul_f32_e32 v61, 0xbfb8aa3b, v57
	v_exp_f32_e32 v61, v61
	s_nop 0
	v_add_f32_e32 v61, 1.0, v61
	v_rcp_f32_e32 v61, v61
	s_nop 0
	v_mul_f32_e32 v57, v57, v61
	v_mul_f32_e32 v61, v56, v57
	v_mov_b32_e32 v56, v62
	v_mov_b32_e32 v57, v58
	v_pk_mul_f32 v[56:57], v[56:57], v[144:145] op_sel_hi:[1,0]
	s_nop 0
	v_mul_f32_e32 v58, 0xbfb8aa3b, v57
	v_exp_f32_e32 v58, v58
	s_nop 0
	v_add_f32_e32 v58, 1.0, v58
	v_rcp_f32_e32 v58, v58
	s_nop 0
	v_mul_f32_e32 v57, v57, v58
	v_mov_b32_e32 v58, v63
	v_mul_f32_e32 v62, v56, v57
	v_pk_mul_f32 v[56:57], v[58:59], v[144:145] op_sel_hi:[1,0]
	s_nop 0
	v_mul_f32_e32 v58, 0xbfb8aa3b, v57
	v_exp_f32_e32 v58, v58
	s_nop 0
	v_add_f32_e32 v58, 1.0, v58
	v_rcp_f32_e32 v58, v58
	s_nop 0
	v_mul_f32_e32 v57, v57, v58
	v_mul_f32_e32 v58, v56, v57
	v_mov_b32_e32 v56, v52
	v_mov_b32_e32 v57, v48
	v_pk_mul_f32 v[56:57], v[56:57], v[144:145] op_sel_hi:[1,0]
	s_nop 0
	v_mul_f32_e32 v48, 0xbfb8aa3b, v57
	v_exp_f32_e32 v48, v48
	s_nop 0
	v_add_f32_e32 v48, 1.0, v48
	v_rcp_f32_e32 v48, v48
	s_nop 0
	v_mul_f32_e32 v48, v57, v48
	v_mul_f32_e32 v52, v56, v48
	v_mov_b32_e32 v48, v53
	v_pk_mul_f32 v[48:49], v[48:49], v[144:145] op_sel_hi:[1,0]
	s_nop 0
	v_mul_f32_e32 v53, 0xbfb8aa3b, v49
	v_exp_f32_e32 v53, v53
	s_nop 0
	v_add_f32_e32 v53, 1.0, v53
	v_rcp_f32_e32 v53, v53
	s_nop 0
	v_mul_f32_e32 v49, v49, v53
	v_mul_f32_e32 v53, v48, v49
	v_mov_b32_e32 v48, v54
	v_mov_b32_e32 v49, v50
	v_pk_mul_f32 v[48:49], v[48:49], v[144:145] op_sel_hi:[1,0]
	s_nop 0
	v_mul_f32_e32 v50, 0xbfb8aa3b, v49
	v_exp_f32_e32 v50, v50
	s_nop 0
	v_add_f32_e32 v50, 1.0, v50
	v_rcp_f32_e32 v50, v50
	s_nop 0
	v_mul_f32_e32 v49, v49, v50
	v_mov_b32_e32 v50, v55
	v_mul_f32_e32 v54, v48, v49
	v_pk_mul_f32 v[48:49], v[50:51], v[144:145] op_sel_hi:[1,0]
	s_nop 0
	v_mul_f32_e32 v50, 0xbfb8aa3b, v49
	v_exp_f32_e32 v50, v50
	s_nop 0
	v_add_f32_e32 v50, 1.0, v50
	v_rcp_f32_e32 v50, v50
	s_nop 0
	v_mul_f32_e32 v49, v49, v50
	v_mul_f32_e32 v51, v48, v49
	v_cvt_pk_bf16_f32 v48, v60, v61
	v_cvt_pk_bf16_f32 v49, v62, v58
	v_cvt_pk_bf16_f32 v50, v52, v53
	v_mad_i64_i32 v[52:53], s[54:55], v142, s58, v[112:113]
	v_lshl_add_u64 v[52:53], v[52:53], 0, s[6:7]
	v_lshl_add_u64 v[52:53], v[52:53], 0, s[16:17]
	v_lshl_add_u64 v[52:53], v[52:53], 0, v[114:115]
	v_cvt_pk_bf16_f32 v51, v54, v51
	global_store_dwordx4 v[52:53], v[48:51], off
	s_nop 1
	v_mov_b32_e32 v48, v44
	v_mov_b32_e32 v49, v40
	v_pk_mul_f32 v[48:49], v[48:49], v[140:141] op_sel_hi:[1,0]
	s_nop 0
	v_mul_f32_e32 v40, 0xbfb8aa3b, v49
	v_exp_f32_e32 v40, v40
	s_nop 0
	v_add_f32_e32 v40, 1.0, v40
	v_rcp_f32_e32 v40, v40
	s_nop 0
	v_mul_f32_e32 v40, v49, v40
	v_mul_f32_e32 v44, v48, v40
	v_mov_b32_e32 v40, v45
	v_pk_mul_f32 v[40:41], v[40:41], v[140:141] op_sel_hi:[1,0]
	s_nop 0
	v_mul_f32_e32 v45, 0xbfb8aa3b, v41
	v_exp_f32_e32 v45, v45
	s_nop 0
	v_add_f32_e32 v45, 1.0, v45
	v_rcp_f32_e32 v45, v45
	s_nop 0
	v_mul_f32_e32 v41, v41, v45
	v_mul_f32_e32 v45, v40, v41
	v_mov_b32_e32 v40, v46
	v_mov_b32_e32 v41, v42
	v_pk_mul_f32 v[40:41], v[40:41], v[140:141] op_sel_hi:[1,0]
	s_nop 0
	v_mul_f32_e32 v42, 0xbfb8aa3b, v41
	v_exp_f32_e32 v42, v42
	s_nop 0
	v_add_f32_e32 v42, 1.0, v42
	v_rcp_f32_e32 v42, v42
	s_nop 0
	v_mul_f32_e32 v41, v41, v42
	v_mov_b32_e32 v42, v47
	v_mul_f32_e32 v46, v40, v41
	v_pk_mul_f32 v[40:41], v[42:43], v[140:141] op_sel_hi:[1,0]
	s_nop 0
	v_mul_f32_e32 v42, 0xbfb8aa3b, v41
	v_exp_f32_e32 v42, v42
	s_nop 0
	v_add_f32_e32 v42, 1.0, v42
	v_rcp_f32_e32 v42, v42
	s_nop 0
	v_mul_f32_e32 v41, v41, v42
	v_mul_f32_e32 v42, v40, v41
	v_mov_b32_e32 v40, v36
	v_mov_b32_e32 v41, v32
	v_pk_mul_f32 v[40:41], v[40:41], v[140:141] op_sel_hi:[1,0]
	s_nop 0
	v_mul_f32_e32 v32, 0xbfb8aa3b, v41
	v_exp_f32_e32 v32, v32
	s_nop 0
	v_add_f32_e32 v32, 1.0, v32
	v_rcp_f32_e32 v32, v32
	s_nop 0
	v_mul_f32_e32 v32, v41, v32
	v_mul_f32_e32 v36, v40, v32
	v_mov_b32_e32 v32, v37
	v_pk_mul_f32 v[32:33], v[32:33], v[140:141] op_sel_hi:[1,0]
	s_nop 0
	v_mul_f32_e32 v37, 0xbfb8aa3b, v33
	v_exp_f32_e32 v37, v37
	s_nop 0
	v_add_f32_e32 v37, 1.0, v37
	v_rcp_f32_e32 v37, v37
	s_nop 0
	v_mul_f32_e32 v33, v33, v37
	v_mul_f32_e32 v37, v32, v33
	v_mov_b32_e32 v32, v38
	v_mov_b32_e32 v33, v34
	v_pk_mul_f32 v[32:33], v[32:33], v[140:141] op_sel_hi:[1,0]
	s_nop 0
	v_mul_f32_e32 v34, 0xbfb8aa3b, v33
	v_exp_f32_e32 v34, v34
	s_nop 0
	v_add_f32_e32 v34, 1.0, v34
	v_rcp_f32_e32 v34, v34
	s_nop 0
	v_mul_f32_e32 v33, v33, v34
	v_mov_b32_e32 v34, v39
	v_mul_f32_e32 v38, v32, v33
; __device__ __forceinline__ float fast_sigmoid(float x) { return __builtin_amdgcn_rcpf(1.f + __builtin_amdgcn_exp2f(-LOG2E * x)); }
; __device__ __forceinline__ u32x4 pack8(const f32x4 a, const f32x4 b) { u32x4 w; w.x = cvt_pk_bf16(a[0], a[1]); w.y = cvt_pk_bf16(a[2], a[3]); w.z = cvt_pk_bf16(b[0], b[1]); w.w = cvt_pk_bf16(b[2], b[3]); return w; }
;     __device__ __forceinline__ void operator()(const f32x4 (&acc)[2][2][4][2], const Unit& u, int wr, int wc, int fr, int fq, const float* pre = nullptr) const {
;     ...
;         for (int ai = 0; ai < 2; ++ai)
; #pragma unroll
;             for (int m = 0; m < 4; ++m) { const int row = EPI_ROWS(ai, m); const float rs = rs8[ai][m], gw = gw8[ai][m];
;                 const float rs2 = rs * gw; f32x4 o[2];
; #pragma unroll
;                 for (int bj = 0; bj < 2; ++bj)
; #pragma unroll
;                     for (int e = 0; e < 4; ++e) { const float a = acc[ai][bj][m][0][e] * rs, b = acc[ai][bj][m][1][e] * rs2; o[bj][e] = a * fast_sigmoid(a) * b; }
;                 if ((MOE && MOE_FP8) || (!MOE && f8)) { u32x2 w; w.x = pk4_fp8(o[0][0], o[0][1], o[0][2], o[0][3]); w.y = pk4_fp8(o[1][0], o[1][1], o[1][2], o[1][3]);
;                     *(u32x2*)((unsigned char*)G + (size_t)row * DFF + u.pn * HALF + wc * 32 + 8 * fq) = w; }
;                 else *(u32x4*)(G + (size_t)row * DFF + u.pn * HALF + wc * 32 + 8 * fq) = pack8(o[0], o[1]); }
	v_pk_mul_f32 v[32:33], v[34:35], v[140:141] op_sel_hi:[1,0]
	s_nop 0
	v_mul_f32_e32 v34, 0xbfb8aa3b, v33
	v_exp_f32_e32 v34, v34
	s_nop 0
	v_add_f32_e32 v34, 1.0, v34
	v_rcp_f32_e32 v34, v34
	s_nop 0
	v_mul_f32_e32 v33, v33, v34
	v_mul_f32_e32 v35, v32, v33
	v_cvt_pk_bf16_f32 v32, v44, v45
	v_cvt_pk_bf16_f32 v33, v46, v42
	v_cvt_pk_bf16_f32 v34, v36, v37
	v_mad_i64_i32 v[36:37], s[54:55], v138, s58, v[112:113]
	v_lshl_add_u64 v[36:37], v[36:37], 0, s[6:7]
	v_lshl_add_u64 v[36:37], v[36:37], 0, s[16:17]
	v_lshl_add_u64 v[36:37], v[36:37], 0, v[114:115]
	v_cvt_pk_bf16_f32 v35, v38, v35
	global_store_dwordx4 v[36:37], v[32:35], off
	s_nop 1
	v_mov_b32_e32 v32, v28
	v_mov_b32_e32 v33, v24
	v_pk_mul_f32 v[32:33], v[32:33], v[136:137] op_sel_hi:[1,0]
	s_nop 0
	v_mul_f32_e32 v24, 0xbfb8aa3b, v33
	v_exp_f32_e32 v24, v24
	s_nop 0
	v_add_f32_e32 v24, 1.0, v24
	v_rcp_f32_e32 v24, v24
	s_nop 0
	v_mul_f32_e32 v24, v33, v24
	v_mul_f32_e32 v28, v32, v24
	v_mov_b32_e32 v24, v29
	v_pk_mul_f32 v[24:25], v[24:25], v[136:137] op_sel_hi:[1,0]
	s_nop 0
	v_mul_f32_e32 v29, 0xbfb8aa3b, v25
	v_exp_f32_e32 v29, v29
	s_nop 0
	v_add_f32_e32 v29, 1.0, v29
	v_rcp_f32_e32 v29, v29
	s_nop 0
	v_mul_f32_e32 v25, v25, v29
	v_mul_f32_e32 v29, v24, v25
	v_mov_b32_e32 v24, v30
	v_mov_b32_e32 v25, v26
	v_pk_mul_f32 v[24:25], v[24:25], v[136:137] op_sel_hi:[1,0]
	s_nop 0
	v_mul_f32_e32 v26, 0xbfb8aa3b, v25
	v_exp_f32_e32 v26, v26
	s_nop 0
	v_add_f32_e32 v26, 1.0, v26
	v_rcp_f32_e32 v26, v26
	s_nop 0
	v_mul_f32_e32 v25, v25, v26
	v_mov_b32_e32 v26, v31
	v_mul_f32_e32 v30, v24, v25
	v_pk_mul_f32 v[24:25], v[26:27], v[136:137] op_sel_hi:[1,0]
	s_nop 0
	v_mul_f32_e32 v26, 0xbfb8aa3b, v25
	v_exp_f32_e32 v26, v26
	s_nop 0
	v_add_f32_e32 v26, 1.0, v26
	v_rcp_f32_e32 v26, v26
	s_nop 0
	v_mul_f32_e32 v25, v25, v26
	v_mul_f32_e32 v26, v24, v25
	v_mov_b32_e32 v24, v20
	v_mov_b32_e32 v25, v16
	v_pk_mul_f32 v[24:25], v[24:25], v[136:137] op_sel_hi:[1,0]
	s_nop 0
	v_mul_f32_e32 v16, 0xbfb8aa3b, v25
	v_exp_f32_e32 v16, v16
	s_nop 0
	v_add_f32_e32 v16, 1.0, v16
	v_rcp_f32_e32 v16, v16
	s_nop 0
	v_mul_f32_e32 v16, v25, v16
	v_mul_f32_e32 v20, v24, v16
	v_mov_b32_e32 v16, v21
	v_pk_mul_f32 v[16:17], v[16:17], v[136:137] op_sel_hi:[1,0]
	s_nop 0
	v_mul_f32_e32 v21, 0xbfb8aa3b, v17
	v_exp_f32_e32 v21, v21
	s_nop 0
	v_add_f32_e32 v21, 1.0, v21
	v_rcp_f32_e32 v21, v21
	s_nop 0
	v_mul_f32_e32 v17, v17, v21
	v_mul_f32_e32 v21, v16, v17
	v_mov_b32_e32 v16, v22
	v_mov_b32_e32 v17, v18
	v_pk_mul_f32 v[16:17], v[16:17], v[136:137] op_sel_hi:[1,0]
	s_nop 0
	v_mul_f32_e32 v18, 0xbfb8aa3b, v17
	v_exp_f32_e32 v18, v18
	s_nop 0
	v_add_f32_e32 v18, 1.0, v18
	v_rcp_f32_e32 v18, v18
	s_nop 0
	v_mul_f32_e32 v17, v17, v18
	v_mov_b32_e32 v18, v23
	v_mul_f32_e32 v22, v16, v17
	v_pk_mul_f32 v[16:17], v[18:19], v[136:137] op_sel_hi:[1,0]
	s_nop 0
	v_mul_f32_e32 v18, 0xbfb8aa3b, v17
	v_exp_f32_e32 v18, v18
	s_nop 0
	v_add_f32_e32 v18, 1.0, v18
	v_rcp_f32_e32 v18, v18
	s_nop 0
	v_mul_f32_e32 v17, v17, v18
	v_mul_f32_e32 v19, v16, v17
	v_cvt_pk_bf16_f32 v16, v28, v29
	v_cvt_pk_bf16_f32 v17, v30, v26
	v_cvt_pk_bf16_f32 v18, v20, v21
	v_mad_i64_i32 v[20:21], s[54:55], v134, s58, v[112:113]
	v_lshl_add_u64 v[20:21], v[20:21], 0, s[6:7]
	v_lshl_add_u64 v[20:21], v[20:21], 0, s[16:17]
	v_lshl_add_u64 v[20:21], v[20:21], 0, v[114:115]
	v_cvt_pk_bf16_f32 v19, v22, v19
	global_store_dwordx4 v[20:21], v[16:19], off
	s_nop 1
	v_mov_b32_e32 v16, v12
	v_mov_b32_e32 v17, v8
	v_pk_mul_f32 v[16:17], v[16:17], v[128:129] op_sel_hi:[1,0]
	s_nop 0
	v_mul_f32_e32 v8, 0xbfb8aa3b, v17
	v_exp_f32_e32 v8, v8
	s_nop 0
	v_add_f32_e32 v8, 1.0, v8
	v_rcp_f32_e32 v8, v8
	s_nop 0
	v_mul_f32_e32 v8, v17, v8
	v_mul_f32_e32 v12, v16, v8
	v_mov_b32_e32 v8, v13
	v_pk_mul_f32 v[8:9], v[8:9], v[128:129] op_sel_hi:[1,0]
	s_nop 0
	v_mul_f32_e32 v13, 0xbfb8aa3b, v9
	v_exp_f32_e32 v13, v13
	s_nop 0
	v_add_f32_e32 v13, 1.0, v13
	v_rcp_f32_e32 v13, v13
	s_nop 0
	v_mul_f32_e32 v9, v9, v13
	v_mul_f32_e32 v13, v8, v9
	v_mov_b32_e32 v8, v14
	v_mov_b32_e32 v9, v10
	v_pk_mul_f32 v[8:9], v[8:9], v[128:129] op_sel_hi:[1,0]
	s_nop 0
	v_mul_f32_e32 v10, 0xbfb8aa3b, v9
	v_exp_f32_e32 v10, v10
	s_nop 0
	v_add_f32_e32 v10, 1.0, v10
	v_rcp_f32_e32 v10, v10
	s_nop 0
	v_mul_f32_e32 v9, v9, v10
	v_mov_b32_e32 v10, v15
	v_mul_f32_e32 v14, v8, v9
	v_pk_mul_f32 v[8:9], v[10:11], v[128:129] op_sel_hi:[1,0]
	s_nop 0
	v_mul_f32_e32 v10, 0xbfb8aa3b, v9
	v_exp_f32_e32 v10, v10
	s_nop 0
	v_add_f32_e32 v10, 1.0, v10
	v_rcp_f32_e32 v10, v10
	s_nop 0
	v_mul_f32_e32 v9, v9, v10
	v_mul_f32_e32 v10, v8, v9
	v_mov_b32_e32 v8, v0
	v_mov_b32_e32 v9, v4
	v_pk_mul_f32 v[8:9], v[8:9], v[128:129] op_sel_hi:[1,0]
	v_mov_b32_e32 v4, v1
	v_mul_f32_e32 v0, 0xbfb8aa3b, v9
	v_exp_f32_e32 v0, v0
	s_nop 0
	v_add_f32_e32 v0, 1.0, v0
	v_rcp_f32_e32 v0, v0
	s_nop 0
	v_mul_f32_e32 v0, v9, v0
	v_mul_f32_e32 v8, v8, v0
	v_pk_mul_f32 v[0:1], v[4:5], v[128:129] op_sel_hi:[1,0]
	s_nop 0
	v_mul_f32_e32 v4, 0xbfb8aa3b, v1
	v_exp_f32_e32 v4, v4
	s_nop 0
	v_add_f32_e32 v4, 1.0, v4
	v_rcp_f32_e32 v4, v4
	s_nop 0
	v_mul_f32_e32 v1, v1, v4
	v_mul_f32_e32 v4, v0, v1
	v_mov_b32_e32 v0, v2
	v_mov_b32_e32 v1, v6
	v_pk_mul_f32 v[0:1], v[0:1], v[128:129] op_sel_hi:[1,0]
	v_mov_b32_e32 v6, v3
	v_mul_f32_e32 v2, 0xbfb8aa3b, v1
	v_exp_f32_e32 v2, v2
	s_nop 0
	v_add_f32_e32 v2, 1.0, v2
	v_rcp_f32_e32 v2, v2
	s_nop 0
	v_mul_f32_e32 v1, v1, v2
	v_mul_f32_e32 v5, v0, v1
	v_pk_mul_f32 v[0:1], v[6:7], v[128:129] op_sel_hi:[1,0]
	s_nop 0
	v_mul_f32_e32 v2, 0xbfb8aa3b, v1
	v_exp_f32_e32 v2, v2
	s_nop 0
	v_add_f32_e32 v2, 1.0, v2
	v_rcp_f32_e32 v2, v2
	s_nop 0
	v_mul_f32_e32 v1, v1, v2
	v_mul_f32_e32 v3, v0, v1
	v_cvt_pk_bf16_f32 v0, v12, v13
	v_cvt_pk_bf16_f32 v1, v14, v10
	v_cvt_pk_bf16_f32 v2, v8, v4
	v_cvt_pk_bf16_f32 v3, v5, v3
	v_mad_i64_i32 v[4:5], s[54:55], v132, s58, v[112:113]
	v_lshl_add_u64 v[4:5], v[4:5], 0, s[6:7]
	v_lshl_add_u64 v[4:5], v[4:5], 0, s[16:17]
	v_lshl_add_u64 v[4:5], v[4:5], 0, v[114:115]
	s_mov_b64 s[6:7], -1
	global_store_dwordx4 v[4:5], v[0:3], off
	s_cbranch_vccnz .LBB0_1623
	s_andn2_b64 vcc, exec, s[2:3]
	v_mov_b32 v0, 0
	s_cbranch_vccnz .LBB0_1622
	s_barrier
	s_branch .LBB0_1622

; __device__ __forceinline__ float opaque_f(float x) { asm volatile("" : "+v"(x)); return x; }
; template <int MASK> __device__ __forceinline__ float swz_f(float v) { return __builtin_bit_cast(float, __builtin_amdgcn_ds_swizzle(__builtin_bit_cast(int, v), (MASK << 10) | 0x1f)); }
; __device__ __forceinline__ float sum_x32(float v) { const unsigned u = __builtin_bit_cast(unsigned, v); auto rr = __builtin_amdgcn_permlane32_swap(u, u, false, false); return __builtin_bit_cast(float, (unsigned)rr[0]) + __builtin_bit_cast(float, (unsigned)rr[1]); }
; __device__ __forceinline__ float rstd_q(const float* ssq, int row, int fq) {
;     const f32x4 p = *(const f32x4*)(ssq + 16 * (size_t)row + 4 * fq); float s = (p.x + p.y) + (p.z + p.w); s += swz_f<16>(s); s = sum_x32(s);
;     return __builtin_amdgcn_rsqf(s * (1.f / 1024.f) + EPS);
;     __device__ __forceinline__ void operator()(const f32x4 (&acc)[2][2][4][2], const Unit& u, int wr, int wc, int fr, int fq, const float* pre = nullptr) const {
;         float rs8[2][4], gw8[2][4];
; #pragma unroll
;         for (int ai = 0; ai < 2; ++ai)
; #pragma unroll
;             for (int m = 0; m < 4; ++m) { const int row = EPI_ROWS(ai, m); float rs, gw = 1.f;
;                 if (MOE) { rs = (MOE_FP8 ? opaque_f(1.f / W13_SCALE) : srs[row]); gw = (HAS_PRE ? pre[ai * 4 + m] : sgw[row]) * (MOE_FP8 ? G8_SCALE : 1.f); } else { rs = rstd_q(ssq, row, fq) * ascale; if (f8) gw = G8_SCALE; }
;                 rs8[ai][m] = rs; gw8[ai][m] = gw; }
.LBB0_1785:
	v_mov_b32_e32 v128, v152
	v_mov_b32_e32 v156, v153
	s_lshl_b32 s6, s58, 8
	s_add_i32 s6, s6, s44
	v_add_u32_e32 v146, s6, v128
	v_lshlrev_b32_e32 v128, 2, v156
	v_ashrrev_i32_e32 v129, 31, v128
	v_ashrrev_i32_e32 v147, 31, v146
	v_lshl_add_u64 v[128:129], v[128:129], 2, s[10:11]
	v_lshlrev_b64 v[130:131], 6, v[146:147]
	v_lshl_add_u64 v[130:131], v[128:129], 0, v[130:131]
	v_add_co_u32_e32 v208, vcc, 0x2000, v130
	global_load_dwordx4 v[180:183], v[130:131], off offset:1024
	global_load_dwordx4 v[184:187], v[130:131], off offset:2048
	v_addc_co_u32_e32 v209, vcc, 0, v131, vcc
	global_load_dwordx4 v[188:191], v[130:131], off offset:3072
	global_load_dwordx4 v[192:195], v[208:209], off
	global_load_dwordx4 v[196:199], v[208:209], off offset:1024
	global_load_dwordx4 v[200:203], v[208:209], off offset:2048
	global_load_dwordx4 v[204:207], v[208:209], off offset:3072
	global_load_dwordx4 v[130:133], v[130:131], off
	v_add_u32_e32 v144, 16, v146
	v_ashrrev_i32_e32 v145, 31, v144
	v_add_u32_e32 v142, 32, v146
	v_ashrrev_i32_e32 v143, 31, v142
	v_add_u32_e32 v140, 48, v146
	v_ashrrev_i32_e32 v141, 31, v140
	v_add_u32_e32 v138, 0x80, v146
	v_ashrrev_i32_e32 v139, 31, v138
	v_add_u32_e32 v136, 0x90, v146
	v_ashrrev_i32_e32 v137, 31, v136
	v_mov_b32_e32 v162, v124
	v_mov_b32_e32 v163, v120
	v_mov_b32_e32 v120, v125
	v_mov_b32_e32 v160, v126
	v_mov_b32_e32 v161, v122
	v_mov_b32_e32 v122, v127
	v_mov_b32_e32 v157, v114
	s_movk_i32 s58, 0xe00
	s_andn2_b64 vcc, exec, s[18:19]
	s_waitcnt vmcnt(0)
	v_mov_b32_e32 v134, v131
	v_mov_b32_e32 v135, v132
	v_mov_b32_e32 v131, v133
	v_pk_add_f32 v[130:131], v[134:135], v[130:131]
	s_nop 0
	v_add_f32_e32 v130, v130, v131
	ds_swizzle_b32 v131, v130 offset:swizzle(SWAP,16)
	s_waitcnt lgkmcnt(0)
	v_add_f32_e32 v130, v130, v131
	v_mov_b32_e32 v131, v130
	s_nop 1
	v_permlane32_swap_b32_e32 v130, v131
	v_add_f32_e32 v130, v130, v131
	v_fmamk_f32 v130, v130, 0x3a800000, v230
	v_rsq_f32_e32 v147, v130
	s_nop 1
	v_mul_f32_e32 v165, 0x3c800000, v147
	v_mul_f32_e32 v164, 0x41000000, v165
	v_pk_mul_f32 v[162:163], v[162:163], v[164:165]
	v_pk_mul_f32 v[120:121], v[120:121], v[164:165]
	s_waitcnt vmcnt(0)
	v_mov_b32_e32 v130, v180
	v_mov_b32_e32 v131, v181
	v_mov_b32_e32 v132, v182
	v_mov_b32_e32 v133, v183
	v_mov_b32_e32 v134, v131
	v_mov_b32_e32 v135, v132
	v_mov_b32_e32 v131, v133
	v_pk_add_f32 v[130:131], v[134:135], v[130:131]
	s_nop 0
	v_add_f32_e32 v130, v130, v131
	ds_swizzle_b32 v131, v130 offset:swizzle(SWAP,16)
	s_waitcnt lgkmcnt(0)
	v_add_f32_e32 v130, v130, v131
	v_mov_b32_e32 v131, v130
	s_nop 1
	v_permlane32_swap_b32_e32 v130, v131
	v_add_f32_e32 v130, v130, v131
	v_fmamk_f32 v130, v130, 0x3a800000, v230
	v_rsq_f32_e32 v145, v130
	s_nop 1
	s_waitcnt vmcnt(0)
	v_mov_b32_e32 v130, v184
	v_mov_b32_e32 v131, v185
	v_mov_b32_e32 v132, v186
	v_mov_b32_e32 v133, v187
	v_mov_b32_e32 v134, v131
	v_mov_b32_e32 v135, v132
	v_mov_b32_e32 v131, v133
	v_pk_add_f32 v[130:131], v[134:135], v[130:131]
	s_nop 0
	v_add_f32_e32 v130, v130, v131
	ds_swizzle_b32 v131, v130 offset:swizzle(SWAP,16)
	s_waitcnt lgkmcnt(0)
	v_add_f32_e32 v130, v130, v131
	v_mov_b32_e32 v131, v130
	s_nop 1
	v_permlane32_swap_b32_e32 v130, v131
	v_add_f32_e32 v130, v130, v131
	v_fmamk_f32 v130, v130, 0x3a800000, v230
	v_rsq_f32_e32 v143, v130
	s_nop 1
	s_waitcnt vmcnt(0)
	v_mov_b32_e32 v130, v188
	v_mov_b32_e32 v131, v189
	v_mov_b32_e32 v132, v190
	v_mov_b32_e32 v133, v191
	v_mov_b32_e32 v134, v131
	v_mov_b32_e32 v135, v132
	v_mov_b32_e32 v131, v133
	v_pk_add_f32 v[130:131], v[134:135], v[130:131]
	s_nop 0
	v_add_f32_e32 v130, v130, v131
	ds_swizzle_b32 v131, v130 offset:swizzle(SWAP,16)
	s_waitcnt lgkmcnt(0)
	v_add_f32_e32 v130, v130, v131
	v_mov_b32_e32 v131, v130
	s_nop 1
	v_permlane32_swap_b32_e32 v130, v131
	v_add_f32_e32 v130, v130, v131
	v_fmamk_f32 v130, v130, 0x3a800000, v230
	v_rsq_f32_e32 v141, v130
	s_nop 1
	s_waitcnt vmcnt(0)
	v_mov_b32_e32 v130, v192
	v_mov_b32_e32 v131, v193
	v_mov_b32_e32 v132, v194
	v_mov_b32_e32 v133, v195
	v_mov_b32_e32 v134, v131
	v_mov_b32_e32 v135, v132
	v_mov_b32_e32 v131, v133
	v_pk_add_f32 v[130:131], v[134:135], v[130:131]
	s_nop 0
	v_add_f32_e32 v130, v130, v131
	ds_swizzle_b32 v131, v130 offset:swizzle(SWAP,16)
	s_waitcnt lgkmcnt(0)
	v_add_f32_e32 v130, v130, v131
	v_mov_b32_e32 v131, v130
	s_nop 1
	v_permlane32_swap_b32_e32 v130, v131
	v_add_f32_e32 v130, v130, v131
	v_fmamk_f32 v130, v130, 0x3a800000, v230
	v_rsq_f32_e32 v139, v130
	s_nop 1
	s_waitcnt vmcnt(0)
	v_mov_b32_e32 v130, v196
	v_mov_b32_e32 v131, v197
	v_mov_b32_e32 v132, v198
	v_mov_b32_e32 v133, v199
	v_mov_b32_e32 v134, v131
	v_mov_b32_e32 v135, v132
	v_mov_b32_e32 v131, v133
	v_pk_add_f32 v[130:131], v[134:135], v[130:131]
	v_add_u32_e32 v134, 0xa0, v146
	v_add_f32_e32 v130, v130, v131
	ds_swizzle_b32 v131, v130 offset:swizzle(SWAP,16)
	v_ashrrev_i32_e32 v135, 31, v134
	s_waitcnt lgkmcnt(0)
	v_add_f32_e32 v130, v130, v131
	v_mov_b32_e32 v131, v130
	s_nop 1
	v_permlane32_swap_b32_e32 v130, v131
	v_add_f32_e32 v130, v130, v131
	v_fmamk_f32 v130, v130, 0x3a800000, v230
	v_rsq_f32_e32 v137, v130
	s_nop 1
	s_waitcnt vmcnt(0)
	v_mov_b32_e32 v130, v200
	v_mov_b32_e32 v131, v201
	v_mov_b32_e32 v132, v202
	v_mov_b32_e32 v133, v203
	v_mov_b32_e32 v158, v131
	v_mov_b32_e32 v159, v132
	v_mov_b32_e32 v131, v133
	v_pk_add_f32 v[130:131], v[158:159], v[130:131]
	v_add_u32_e32 v132, 0xb0, v146
	v_add_f32_e32 v130, v130, v131
	ds_swizzle_b32 v131, v130 offset:swizzle(SWAP,16)
	v_ashrrev_i32_e32 v133, 31, v132
	s_waitcnt lgkmcnt(0)
	v_add_f32_e32 v130, v130, v131
	v_mov_b32_e32 v131, v130
	s_nop 1
	v_permlane32_swap_b32_e32 v130, v131
	v_add_f32_e32 v130, v130, v131
	v_fmamk_f32 v130, v130, 0x3a800000, v230
	v_rsq_f32_e32 v135, v130
	s_nop 1
	s_waitcnt vmcnt(0)
; __device__ __forceinline__ float fast_sigmoid(float x) { return __builtin_amdgcn_rcpf(1.f + __builtin_amdgcn_exp2f(-LOG2E * x)); }
;     __device__ __forceinline__ void operator()(const f32x4 (&acc)[2][2][4][2], const Unit& u, int wr, int wc, int fr, int fq, const float* pre = nullptr) const {
;     ...
;         for (int ai = 0; ai < 2; ++ai)
; #pragma unroll
;             for (int m = 0; m < 4; ++m) { const int row = EPI_ROWS(ai, m); const float rs = rs8[ai][m], gw = gw8[ai][m];
;                 const float rs2 = rs * gw; f32x4 o[2];
; #pragma unroll
;                 for (int bj = 0; bj < 2; ++bj)
; #pragma unroll
;                     for (int e = 0; e < 4; ++e) { const float a = acc[ai][bj][m][0][e] * rs, b = acc[ai][bj][m][1][e] * rs2; o[bj][e] = a * fast_sigmoid(a) * b; }
;                 if ((MOE && MOE_FP8) || (!MOE && f8)) { u32x2 w; w.x = pk4_fp8(o[0][0], o[0][1], o[0][2], o[0][3]); w.y = pk4_fp8(o[1][0], o[1][1], o[1][2], o[1][3]);
;                     *(u32x2*)((unsigned char*)G + (size_t)row * DFF + u.pn * HALF + wc * 32 + 8 * fq) = w; }
	v_mov_b32_e32 v128, v204
	v_mov_b32_e32 v129, v205
	v_mov_b32_e32 v130, v206
	v_mov_b32_e32 v131, v207
	v_mov_b32_e32 v158, v129
	v_mov_b32_e32 v159, v130
	v_mov_b32_e32 v129, v131
	v_pk_add_f32 v[128:129], v[158:159], v[128:129]
	v_mov_b32_e32 v159, v112
	v_mul_f32_e32 v112, 0xbfb8aa3b, v163
	v_exp_f32_e32 v112, v112
	v_add_f32_e32 v128, v128, v129
	v_mov_b32_e32 v158, v116
	ds_swizzle_b32 v129, v128 offset:swizzle(SWAP,16)
	v_add_f32_e32 v112, 1.0, v112
	v_rcp_f32_e32 v112, v112
	s_waitcnt lgkmcnt(0)
	v_add_f32_e32 v128, v128, v129
	v_mul_f32_e32 v112, v163, v112
	v_mul_f32_e32 v116, v162, v112
	v_mul_f32_e32 v112, 0xbfb8aa3b, v121
	v_exp_f32_e32 v112, v112
	v_mov_b32_e32 v129, v128
	s_nop 1
	v_permlane32_swap_b32_e32 v128, v129
	v_add_f32_e32 v112, 1.0, v112
	v_rcp_f32_e32 v112, v112
	v_add_f32_e32 v128, v128, v129
	v_fmamk_f32 v128, v128, 0x3a800000, v230
	v_rsq_f32_e32 v130, v128
	v_mul_f32_e32 v112, v121, v112
	v_lshlrev_b32_e32 v128, 3, v156
	v_mov_b32_e32 v156, v118
	v_mul_f32_e32 v118, v120, v112
	v_pk_mul_f32 v[120:121], v[160:161], v[164:165]
	v_ashrrev_i32_e32 v129, 31, v128
	v_mul_f32_e32 v112, 0xbfb8aa3b, v121
	v_exp_f32_e32 v112, v112
	s_nop 0
	v_add_f32_e32 v112, 1.0, v112
	v_rcp_f32_e32 v112, v112
	s_nop 0
	v_mul_f32_e32 v112, v121, v112
	v_mul_f32_e32 v124, v120, v112
	v_pk_mul_f32 v[120:121], v[122:123], v[164:165]
	v_mul_f32_e32 v123, 0x3c800000, v145
	v_mul_f32_e32 v112, 0xbfb8aa3b, v121
	v_exp_f32_e32 v112, v112
	s_nop 0
	v_add_f32_e32 v112, 1.0, v112
	v_rcp_f32_e32 v112, v112
	s_nop 0
	v_mul_f32_e32 v112, v121, v112
	v_mul_f32_e32 v122, v120, v112
	v_pk_mul_f32 v[120:121], v[158:159], v[164:165]
	s_nop 0
	v_mul_f32_e32 v112, 0xbfb8aa3b, v121
	v_exp_f32_e32 v112, v112
	s_nop 0
	v_add_f32_e32 v112, 1.0, v112
	v_rcp_f32_e32 v112, v112
	s_nop 0
	v_mul_f32_e32 v112, v121, v112
	v_mul_f32_e32 v120, v120, v112
	v_mov_b32_e32 v112, v117
	v_pk_mul_f32 v[112:113], v[112:113], v[164:165]
	s_nop 0
	v_mul_f32_e32 v114, 0xbfb8aa3b, v113
	v_exp_f32_e32 v114, v114
	s_nop 0
	v_add_f32_e32 v114, 1.0, v114
	v_rcp_f32_e32 v114, v114
	s_nop 0
	v_mul_f32_e32 v113, v113, v114
	v_mul_f32_e32 v117, v112, v113
	v_pk_mul_f32 v[112:113], v[156:157], v[164:165]
	s_nop 0
	v_mul_f32_e32 v114, 0xbfb8aa3b, v113
	v_exp_f32_e32 v114, v114
	s_nop 0
	v_add_f32_e32 v114, 1.0, v114
	v_rcp_f32_e32 v114, v114
	s_nop 0
	v_mul_f32_e32 v113, v113, v114
	v_mov_b32_e32 v114, v119
	v_mul_f32_e32 v121, v112, v113
	v_pk_mul_f32 v[112:113], v[114:115], v[164:165]
	v_med3_f32 v115, v124, s49, v254
	v_mul_f32_e32 v114, 0xbfb8aa3b, v113
	v_exp_f32_e32 v114, v114
	v_mov_b32_e32 v119, v106
	v_mov_b32_e32 v106, v111
	v_add_f32_e32 v114, 1.0, v114
	v_rcp_f32_e32 v114, v114
	s_nop 0
	v_mul_f32_e32 v113, v113, v114
	v_mul_f32_e32 v112, v112, v113
	v_med3_f32 v114, v116, s49, v254
	v_med3_f32 v113, v118, s49, v254
	v_cvt_pk_fp8_f32 v114, v114, v113
	v_med3_f32 v116, v122, s49, v254
	v_med3_f32 v113, v117, s49, v254
	v_med3_f32 v112, v112, s49, v254
	v_cvt_pk_fp8_f32 v114, v115, v116 op_sel:[0,0,1]
	v_med3_f32 v115, v120, s49, v254
	v_cvt_pk_fp8_f32 v115, v115, v113
	v_med3_f32 v116, v121, s49, v254
	v_mov_b32_e32 v120, v108
	v_mov_b32_e32 v121, v104
	v_cvt_pk_fp8_f32 v115, v116, v112 op_sel:[0,0,1]
	v_mov_b64_e32 v[112:113], s[8:9]
	v_mad_i64_i32 v[116:117], s[6:7], v146, s58, v[112:113]
	s_lshl_b32 s6, s57, 7
	s_ashr_i32 s7, s6, 31
	v_lshl_add_u64 v[116:117], v[116:117], 0, s[6:7]
	v_lshl_add_u64 v[116:117], v[116:117], 0, s[12:13]
	v_mul_f32_e32 v122, 0x41000000, v123
	v_lshl_add_u64 v[116:117], v[116:117], 0, v[128:129]
	v_pk_mul_f32 v[120:121], v[120:121], v[122:123]
	global_store_dwordx2 v[116:117], v[114:115], off
	v_mov_b32_e32 v117, v96
	v_mul_f32_e32 v96, 0xbfb8aa3b, v121
	v_exp_f32_e32 v96, v96
	v_mov_b32_e32 v104, v109
	v_pk_mul_f32 v[104:105], v[104:105], v[122:123]
	v_mov_b32_e32 v116, v100
	v_add_f32_e32 v96, 1.0, v96
	v_rcp_f32_e32 v96, v96
	v_mov_b32_e32 v118, v110
	v_mov_b32_e32 v114, v102
	v_mov_b32_e32 v115, v98
	v_mul_f32_e32 v96, v121, v96
	v_mul_f32_e32 v100, v120, v96
	v_mul_f32_e32 v96, 0xbfb8aa3b, v105
	v_exp_f32_e32 v96, v96
	s_nop 0
	v_add_f32_e32 v96, 1.0, v96
	v_rcp_f32_e32 v96, v96
	s_nop 0
	v_mul_f32_e32 v96, v105, v96
	v_mul_f32_e32 v102, v104, v96
	v_pk_mul_f32 v[104:105], v[118:119], v[122:123]
	s_nop 0
	v_mul_f32_e32 v96, 0xbfb8aa3b, v105
	v_exp_f32_e32 v96, v96
	s_nop 0
	v_add_f32_e32 v96, 1.0, v96
	v_rcp_f32_e32 v96, v96
	s_nop 0
	v_mul_f32_e32 v96, v105, v96
	v_mul_f32_e32 v108, v104, v96
	v_pk_mul_f32 v[104:105], v[106:107], v[122:123]
	s_nop 0
	v_mul_f32_e32 v96, 0xbfb8aa3b, v105
	v_exp_f32_e32 v96, v96
	s_nop 0
	v_add_f32_e32 v96, 1.0, v96
	v_rcp_f32_e32 v96, v96
	s_nop 0
	v_mul_f32_e32 v96, v105, v96
	v_mul_f32_e32 v106, v104, v96
	v_pk_mul_f32 v[104:105], v[116:117], v[122:123]
	s_nop 0
	v_mul_f32_e32 v96, 0xbfb8aa3b, v105
	v_exp_f32_e32 v96, v96
	s_nop 0
	v_add_f32_e32 v96, 1.0, v96
	v_rcp_f32_e32 v96, v96
	s_nop 0
	v_mul_f32_e32 v96, v105, v96
	v_mul_f32_e32 v104, v104, v96
	v_mov_b32_e32 v96, v101
	v_pk_mul_f32 v[96:97], v[96:97], v[122:123]
	s_nop 0
	v_mul_f32_e32 v98, 0xbfb8aa3b, v97
	v_exp_f32_e32 v98, v98
	s_nop 0
	v_add_f32_e32 v98, 1.0, v98
	v_rcp_f32_e32 v98, v98
	s_nop 0
	v_mul_f32_e32 v97, v97, v98
	v_mul_f32_e32 v101, v96, v97
	v_pk_mul_f32 v[96:97], v[114:115], v[122:123]
	s_nop 0
	v_mul_f32_e32 v98, 0xbfb8aa3b, v97
	v_exp_f32_e32 v98, v98
	s_nop 0
	v_add_f32_e32 v98, 1.0, v98
	v_rcp_f32_e32 v98, v98
	s_nop 0
	v_mul_f32_e32 v97, v97, v98
	v_mov_b32_e32 v98, v103
	v_mul_f32_e32 v105, v96, v97
	v_pk_mul_f32 v[96:97], v[98:99], v[122:123]
	v_med3_f32 v99, v108, s49, v254
	v_mul_f32_e32 v98, 0xbfb8aa3b, v97
; __device__ __forceinline__ float fast_sigmoid(float x) { return __builtin_amdgcn_rcpf(1.f + __builtin_amdgcn_exp2f(-LOG2E * x)); }
;     __device__ __forceinline__ void operator()(const f32x4 (&acc)[2][2][4][2], const Unit& u, int wr, int wc, int fr, int fq, const float* pre = nullptr) const {
;     ...
;         for (int ai = 0; ai < 2; ++ai)
; #pragma unroll
;             for (int m = 0; m < 4; ++m) { const int row = EPI_ROWS(ai, m); const float rs = rs8[ai][m], gw = gw8[ai][m];
;                 const float rs2 = rs * gw; f32x4 o[2];
; #pragma unroll
;                 for (int bj = 0; bj < 2; ++bj)
; #pragma unroll
;                     for (int e = 0; e < 4; ++e) { const float a = acc[ai][bj][m][0][e] * rs, b = acc[ai][bj][m][1][e] * rs2; o[bj][e] = a * fast_sigmoid(a) * b; }
;                 if ((MOE && MOE_FP8) || (!MOE && f8)) { u32x2 w; w.x = pk4_fp8(o[0][0], o[0][1], o[0][2], o[0][3]); w.y = pk4_fp8(o[1][0], o[1][1], o[1][2], o[1][3]);
;                     *(u32x2*)((unsigned char*)G + (size_t)row * DFF + u.pn * HALF + wc * 32 + 8 * fq) = w; }
	v_exp_f32_e32 v98, v98
	v_mov_b32_e32 v103, v88
	v_mov_b32_e32 v88, v93
	v_add_f32_e32 v98, 1.0, v98
	v_rcp_f32_e32 v98, v98
	s_nop 0
	v_mul_f32_e32 v97, v97, v98
	v_mul_f32_e32 v98, v96, v97
	v_med3_f32 v96, v100, s49, v254
	v_med3_f32 v97, v102, s49, v254
	v_cvt_pk_fp8_f32 v96, v96, v97
	v_med3_f32 v100, v106, s49, v254
	v_med3_f32 v97, v104, s49, v254
	v_med3_f32 v98, v98, s49, v254
	v_cvt_pk_fp8_f32 v96, v99, v100 op_sel:[0,0,1]
	v_med3_f32 v99, v101, s49, v254
	v_cvt_pk_fp8_f32 v97, v97, v99
	v_med3_f32 v100, v105, s49, v254
	v_mul_f32_e32 v105, 0x3c800000, v143
	v_mov_b32_e32 v102, v92
	v_cvt_pk_fp8_f32 v97, v100, v98 op_sel:[0,0,1]
	v_mad_i64_i32 v[98:99], s[54:55], v144, s58, v[112:113]
	v_lshl_add_u64 v[98:99], v[98:99], 0, s[6:7]
	v_lshl_add_u64 v[98:99], v[98:99], 0, s[12:13]
	v_mul_f32_e32 v104, 0x41000000, v105
	v_lshl_add_u64 v[98:99], v[98:99], 0, v[128:129]
	v_pk_mul_f32 v[102:103], v[102:103], v[104:105]
	global_store_dwordx2 v[98:99], v[96:97], off
	v_mov_b32_e32 v99, v80
	v_mul_f32_e32 v80, 0xbfb8aa3b, v103
	v_exp_f32_e32 v80, v80
	v_pk_mul_f32 v[88:89], v[88:89], v[104:105]
	v_mov_b32_e32 v98, v84
	v_mov_b32_e32 v100, v94
	v_add_f32_e32 v80, 1.0, v80
	v_rcp_f32_e32 v80, v80
	v_mov_b32_e32 v101, v90
	v_mov_b32_e32 v96, v86
	v_mov_b32_e32 v90, v95
	v_mul_f32_e32 v80, v103, v80
	v_mul_f32_e32 v84, v102, v80
	v_mul_f32_e32 v80, 0xbfb8aa3b, v89
	v_exp_f32_e32 v80, v80
	v_mov_b32_e32 v97, v82
	v_add_f32_e32 v80, 1.0, v80
	v_rcp_f32_e32 v80, v80
	s_nop 0
	v_mul_f32_e32 v80, v89, v80
	v_mul_f32_e32 v86, v88, v80
	v_pk_mul_f32 v[88:89], v[100:101], v[104:105]
	s_nop 0
	v_mul_f32_e32 v80, 0xbfb8aa3b, v89
	v_exp_f32_e32 v80, v80
	s_nop 0
	v_add_f32_e32 v80, 1.0, v80
	v_rcp_f32_e32 v80, v80
	s_nop 0
	v_mul_f32_e32 v80, v89, v80
	v_mul_f32_e32 v92, v88, v80
	v_pk_mul_f32 v[88:89], v[90:91], v[104:105]
	s_nop 0
	v_mul_f32_e32 v80, 0xbfb8aa3b, v89
	v_exp_f32_e32 v80, v80
	s_nop 0
	v_add_f32_e32 v80, 1.0, v80
	v_rcp_f32_e32 v80, v80
	s_nop 0
	v_mul_f32_e32 v80, v89, v80
	v_mul_f32_e32 v90, v88, v80
	v_pk_mul_f32 v[88:89], v[98:99], v[104:105]
	s_nop 0
	v_mul_f32_e32 v80, 0xbfb8aa3b, v89
	v_exp_f32_e32 v80, v80
	s_nop 0
	v_add_f32_e32 v80, 1.0, v80
	v_rcp_f32_e32 v80, v80
	s_nop 0
	v_mul_f32_e32 v80, v89, v80
	v_mul_f32_e32 v88, v88, v80
	v_mov_b32_e32 v80, v85
	v_pk_mul_f32 v[80:81], v[80:81], v[104:105]
	s_nop 0
	v_mul_f32_e32 v82, 0xbfb8aa3b, v81
	v_exp_f32_e32 v82, v82
	s_nop 0
	v_add_f32_e32 v82, 1.0, v82
	v_rcp_f32_e32 v82, v82
	s_nop 0
	v_mul_f32_e32 v81, v81, v82
	v_mul_f32_e32 v85, v80, v81
	v_pk_mul_f32 v[80:81], v[96:97], v[104:105]
	s_nop 0
	v_mul_f32_e32 v82, 0xbfb8aa3b, v81
	v_exp_f32_e32 v82, v82
	s_nop 0
	v_add_f32_e32 v82, 1.0, v82
	v_rcp_f32_e32 v82, v82
	s_nop 0
	v_mul_f32_e32 v81, v81, v82
	v_mov_b32_e32 v82, v87
	v_mul_f32_e32 v89, v80, v81
	v_pk_mul_f32 v[80:81], v[82:83], v[104:105]
	v_med3_f32 v83, v92, s49, v254
	v_mul_f32_e32 v82, 0xbfb8aa3b, v81
	v_exp_f32_e32 v82, v82
	v_mov_b32_e32 v87, v72
	v_mov_b32_e32 v72, v77
	v_add_f32_e32 v82, 1.0, v82
	v_rcp_f32_e32 v82, v82
	s_nop 0
	v_mul_f32_e32 v81, v81, v82
	v_mul_f32_e32 v82, v80, v81
	v_med3_f32 v80, v84, s49, v254
	v_med3_f32 v81, v86, s49, v254
	v_cvt_pk_fp8_f32 v80, v80, v81
	v_med3_f32 v84, v90, s49, v254
	v_med3_f32 v81, v88, s49, v254
	v_med3_f32 v82, v82, s49, v254
	v_cvt_pk_fp8_f32 v80, v83, v84 op_sel:[0,0,1]
	v_med3_f32 v83, v85, s49, v254
	v_cvt_pk_fp8_f32 v81, v81, v83
	v_med3_f32 v84, v89, s49, v254
	v_mul_f32_e32 v89, 0x3c800000, v141
	v_mov_b32_e32 v86, v76
	v_cvt_pk_fp8_f32 v81, v84, v82 op_sel:[0,0,1]
	v_mad_i64_i32 v[82:83], s[54:55], v142, s58, v[112:113]
	v_lshl_add_u64 v[82:83], v[82:83], 0, s[6:7]
	v_lshl_add_u64 v[82:83], v[82:83], 0, s[12:13]
	v_mul_f32_e32 v88, 0x41000000, v89
	v_lshl_add_u64 v[82:83], v[82:83], 0, v[128:129]
	v_pk_mul_f32 v[86:87], v[86:87], v[88:89]
	global_store_dwordx2 v[82:83], v[80:81], off
	v_mov_b32_e32 v83, v64
	v_mul_f32_e32 v64, 0xbfb8aa3b, v87
	v_exp_f32_e32 v64, v64
	v_pk_mul_f32 v[72:73], v[72:73], v[88:89]
	v_mov_b32_e32 v82, v68
	v_mov_b32_e32 v84, v78
	v_add_f32_e32 v64, 1.0, v64
	v_rcp_f32_e32 v64, v64
	v_mov_b32_e32 v85, v74
	v_mov_b32_e32 v80, v70
	v_mov_b32_e32 v74, v79
	v_mul_f32_e32 v64, v87, v64
	v_mul_f32_e32 v68, v86, v64
	v_mul_f32_e32 v64, 0xbfb8aa3b, v73
	v_exp_f32_e32 v64, v64
	v_mov_b32_e32 v81, v66
	v_add_f32_e32 v64, 1.0, v64
	v_rcp_f32_e32 v64, v64
	s_nop 0
	v_mul_f32_e32 v64, v73, v64
	v_mul_f32_e32 v70, v72, v64
	v_pk_mul_f32 v[72:73], v[84:85], v[88:89]
	s_nop 0
	v_mul_f32_e32 v64, 0xbfb8aa3b, v73
	v_exp_f32_e32 v64, v64
	s_nop 0
	v_add_f32_e32 v64, 1.0, v64
	v_rcp_f32_e32 v64, v64
	s_nop 0
	v_mul_f32_e32 v64, v73, v64
	v_mul_f32_e32 v76, v72, v64
	v_pk_mul_f32 v[72:73], v[74:75], v[88:89]
	s_nop 0
	v_mul_f32_e32 v64, 0xbfb8aa3b, v73
	v_exp_f32_e32 v64, v64
	s_nop 0
	v_add_f32_e32 v64, 1.0, v64
	v_rcp_f32_e32 v64, v64
	s_nop 0
	v_mul_f32_e32 v64, v73, v64
	v_mul_f32_e32 v74, v72, v64
	v_pk_mul_f32 v[72:73], v[82:83], v[88:89]
	s_nop 0
	v_mul_f32_e32 v64, 0xbfb8aa3b, v73
	v_exp_f32_e32 v64, v64
	s_nop 0
	v_add_f32_e32 v64, 1.0, v64
	v_rcp_f32_e32 v64, v64
	s_nop 0
	v_mul_f32_e32 v64, v73, v64
	v_mul_f32_e32 v72, v72, v64
	v_mov_b32_e32 v64, v69
	v_pk_mul_f32 v[64:65], v[64:65], v[88:89]
	s_nop 0
	v_mul_f32_e32 v66, 0xbfb8aa3b, v65
	v_exp_f32_e32 v66, v66
	s_nop 0
	v_add_f32_e32 v66, 1.0, v66
	v_rcp_f32_e32 v66, v66
	s_nop 0
	v_mul_f32_e32 v65, v65, v66
	v_mul_f32_e32 v69, v64, v65
	v_pk_mul_f32 v[64:65], v[80:81], v[88:89]
	s_nop 0
	v_mul_f32_e32 v66, 0xbfb8aa3b, v65
	v_exp_f32_e32 v66, v66
	s_nop 0
	v_add_f32_e32 v66, 1.0, v66
	v_rcp_f32_e32 v66, v66
	s_nop 0
	v_mul_f32_e32 v65, v65, v66
; __device__ __forceinline__ float fast_sigmoid(float x) { return __builtin_amdgcn_rcpf(1.f + __builtin_amdgcn_exp2f(-LOG2E * x)); }
;     __device__ __forceinline__ void operator()(const f32x4 (&acc)[2][2][4][2], const Unit& u, int wr, int wc, int fr, int fq, const float* pre = nullptr) const {
;     ...
;         for (int ai = 0; ai < 2; ++ai)
; #pragma unroll
;             for (int m = 0; m < 4; ++m) { const int row = EPI_ROWS(ai, m); const float rs = rs8[ai][m], gw = gw8[ai][m];
;                 const float rs2 = rs * gw; f32x4 o[2];
; #pragma unroll
;                 for (int bj = 0; bj < 2; ++bj)
; #pragma unroll
;                     for (int e = 0; e < 4; ++e) { const float a = acc[ai][bj][m][0][e] * rs, b = acc[ai][bj][m][1][e] * rs2; o[bj][e] = a * fast_sigmoid(a) * b; }
;                 if ((MOE && MOE_FP8) || (!MOE && f8)) { u32x2 w; w.x = pk4_fp8(o[0][0], o[0][1], o[0][2], o[0][3]); w.y = pk4_fp8(o[1][0], o[1][1], o[1][2], o[1][3]);
;                     *(u32x2*)((unsigned char*)G + (size_t)row * DFF + u.pn * HALF + wc * 32 + 8 * fq) = w; }
	v_mov_b32_e32 v66, v71
	v_mul_f32_e32 v73, v64, v65
	v_pk_mul_f32 v[64:65], v[66:67], v[88:89]
	v_med3_f32 v67, v76, s49, v254
	v_mul_f32_e32 v66, 0xbfb8aa3b, v65
	v_exp_f32_e32 v66, v66
	v_mov_b32_e32 v71, v56
	v_mov_b32_e32 v56, v61
	v_add_f32_e32 v66, 1.0, v66
	v_rcp_f32_e32 v66, v66
	s_nop 0
	v_mul_f32_e32 v65, v65, v66
	v_mul_f32_e32 v66, v64, v65
	v_med3_f32 v64, v68, s49, v254
	v_med3_f32 v65, v70, s49, v254
	v_cvt_pk_fp8_f32 v64, v64, v65
	v_med3_f32 v68, v74, s49, v254
	v_med3_f32 v65, v72, s49, v254
	v_med3_f32 v66, v66, s49, v254
	v_cvt_pk_fp8_f32 v64, v67, v68 op_sel:[0,0,1]
	v_med3_f32 v67, v69, s49, v254
	v_cvt_pk_fp8_f32 v65, v65, v67
	v_med3_f32 v68, v73, s49, v254
	v_mul_f32_e32 v73, 0x3c800000, v139
	v_mov_b32_e32 v70, v60
	v_cvt_pk_fp8_f32 v65, v68, v66 op_sel:[0,0,1]
	v_mad_i64_i32 v[66:67], s[54:55], v140, s58, v[112:113]
	v_lshl_add_u64 v[66:67], v[66:67], 0, s[6:7]
	v_lshl_add_u64 v[66:67], v[66:67], 0, s[12:13]
	v_mul_f32_e32 v72, 0x41000000, v73
	v_lshl_add_u64 v[66:67], v[66:67], 0, v[128:129]
	v_pk_mul_f32 v[70:71], v[70:71], v[72:73]
	global_store_dwordx2 v[66:67], v[64:65], off
	v_mov_b32_e32 v67, v48
	v_mul_f32_e32 v48, 0xbfb8aa3b, v71
	v_exp_f32_e32 v48, v48
	v_pk_mul_f32 v[56:57], v[56:57], v[72:73]
	v_mov_b32_e32 v66, v52
	v_mov_b32_e32 v68, v62
	v_add_f32_e32 v48, 1.0, v48
	v_rcp_f32_e32 v48, v48
	v_mov_b32_e32 v69, v58
	v_mov_b32_e32 v64, v54
	v_mov_b32_e32 v58, v63
	v_mul_f32_e32 v48, v71, v48
	v_mul_f32_e32 v52, v70, v48
	v_mul_f32_e32 v48, 0xbfb8aa3b, v57
	v_exp_f32_e32 v48, v48
	v_mov_b32_e32 v65, v50
	v_add_f32_e32 v48, 1.0, v48
	v_rcp_f32_e32 v48, v48
	s_nop 0
	v_mul_f32_e32 v48, v57, v48
	v_mul_f32_e32 v54, v56, v48
	v_pk_mul_f32 v[56:57], v[68:69], v[72:73]
	s_nop 0
	v_mul_f32_e32 v48, 0xbfb8aa3b, v57
	v_exp_f32_e32 v48, v48
	s_nop 0
	v_add_f32_e32 v48, 1.0, v48
	v_rcp_f32_e32 v48, v48
	s_nop 0
	v_mul_f32_e32 v48, v57, v48
	v_mul_f32_e32 v60, v56, v48
	v_pk_mul_f32 v[56:57], v[58:59], v[72:73]
	s_nop 0
	v_mul_f32_e32 v48, 0xbfb8aa3b, v57
	v_exp_f32_e32 v48, v48
	s_nop 0
	v_add_f32_e32 v48, 1.0, v48
	v_rcp_f32_e32 v48, v48
	s_nop 0
	v_mul_f32_e32 v48, v57, v48
	v_mul_f32_e32 v58, v56, v48
	v_pk_mul_f32 v[56:57], v[66:67], v[72:73]
	s_nop 0
	v_mul_f32_e32 v48, 0xbfb8aa3b, v57
	v_exp_f32_e32 v48, v48
	s_nop 0
	v_add_f32_e32 v48, 1.0, v48
	v_rcp_f32_e32 v48, v48
	s_nop 0
	v_mul_f32_e32 v48, v57, v48
	v_mul_f32_e32 v56, v56, v48
	v_mov_b32_e32 v48, v53
	v_pk_mul_f32 v[48:49], v[48:49], v[72:73]
	s_nop 0
	v_mul_f32_e32 v50, 0xbfb8aa3b, v49
	v_exp_f32_e32 v50, v50
	s_nop 0
	v_add_f32_e32 v50, 1.0, v50
	v_rcp_f32_e32 v50, v50
	s_nop 0
	v_mul_f32_e32 v49, v49, v50
	v_mul_f32_e32 v53, v48, v49
	v_pk_mul_f32 v[48:49], v[64:65], v[72:73]
	s_nop 0
	v_mul_f32_e32 v50, 0xbfb8aa3b, v49
	v_exp_f32_e32 v50, v50
	s_nop 0
	v_add_f32_e32 v50, 1.0, v50
	v_rcp_f32_e32 v50, v50
	s_nop 0
	v_mul_f32_e32 v49, v49, v50
	v_mov_b32_e32 v50, v55
	v_mul_f32_e32 v57, v48, v49
	v_pk_mul_f32 v[48:49], v[50:51], v[72:73]
	v_med3_f32 v51, v60, s49, v254
	v_mul_f32_e32 v50, 0xbfb8aa3b, v49
	v_exp_f32_e32 v50, v50
	v_mov_b32_e32 v55, v40
	v_mov_b32_e32 v40, v45
	v_add_f32_e32 v50, 1.0, v50
	v_rcp_f32_e32 v50, v50
	s_nop 0
	v_mul_f32_e32 v49, v49, v50
	v_mul_f32_e32 v50, v48, v49
	v_med3_f32 v48, v52, s49, v254
	v_med3_f32 v49, v54, s49, v254
	v_cvt_pk_fp8_f32 v48, v48, v49
	v_med3_f32 v52, v58, s49, v254
	v_med3_f32 v49, v56, s49, v254
	v_med3_f32 v50, v50, s49, v254
	v_cvt_pk_fp8_f32 v48, v51, v52 op_sel:[0,0,1]
	v_med3_f32 v51, v53, s49, v254
	v_cvt_pk_fp8_f32 v49, v49, v51
	v_med3_f32 v52, v57, s49, v254
	v_mul_f32_e32 v57, 0x3c800000, v137
	v_mov_b32_e32 v54, v44
	v_cvt_pk_fp8_f32 v49, v52, v50 op_sel:[0,0,1]
	v_mad_i64_i32 v[50:51], s[54:55], v138, s58, v[112:113]
	v_lshl_add_u64 v[50:51], v[50:51], 0, s[6:7]
	v_lshl_add_u64 v[50:51], v[50:51], 0, s[12:13]
	v_mul_f32_e32 v56, 0x41000000, v57
	v_lshl_add_u64 v[50:51], v[50:51], 0, v[128:129]
	v_pk_mul_f32 v[54:55], v[54:55], v[56:57]
	global_store_dwordx2 v[50:51], v[48:49], off
	v_mov_b32_e32 v51, v32
	v_mul_f32_e32 v32, 0xbfb8aa3b, v55
	v_exp_f32_e32 v32, v32
	v_pk_mul_f32 v[40:41], v[40:41], v[56:57]
	v_mov_b32_e32 v50, v36
	v_mov_b32_e32 v52, v46
	v_add_f32_e32 v32, 1.0, v32
	v_rcp_f32_e32 v32, v32
	v_mov_b32_e32 v53, v42
	v_mov_b32_e32 v48, v38
	v_mov_b32_e32 v42, v47
	v_mul_f32_e32 v32, v55, v32
	v_mul_f32_e32 v36, v54, v32
	v_mul_f32_e32 v32, 0xbfb8aa3b, v41
	v_exp_f32_e32 v32, v32
	v_mov_b32_e32 v49, v34
	v_add_f32_e32 v32, 1.0, v32
	v_rcp_f32_e32 v32, v32
	s_nop 0
	v_mul_f32_e32 v32, v41, v32
	v_mul_f32_e32 v38, v40, v32
	v_pk_mul_f32 v[40:41], v[52:53], v[56:57]
	s_nop 0
	v_mul_f32_e32 v32, 0xbfb8aa3b, v41
	v_exp_f32_e32 v32, v32
	s_nop 0
	v_add_f32_e32 v32, 1.0, v32
	v_rcp_f32_e32 v32, v32
	s_nop 0
	v_mul_f32_e32 v32, v41, v32
	v_mul_f32_e32 v44, v40, v32
	v_pk_mul_f32 v[40:41], v[42:43], v[56:57]
	s_nop 0
	v_mul_f32_e32 v32, 0xbfb8aa3b, v41
	v_exp_f32_e32 v32, v32
	s_nop 0
	v_add_f32_e32 v32, 1.0, v32
	v_rcp_f32_e32 v32, v32
	s_nop 0
	v_mul_f32_e32 v32, v41, v32
	v_mul_f32_e32 v42, v40, v32
	v_pk_mul_f32 v[40:41], v[50:51], v[56:57]
	s_nop 0
	v_mul_f32_e32 v32, 0xbfb8aa3b, v41
	v_exp_f32_e32 v32, v32
	s_nop 0
	v_add_f32_e32 v32, 1.0, v32
	v_rcp_f32_e32 v32, v32
	s_nop 0
	v_mul_f32_e32 v32, v41, v32
	v_mul_f32_e32 v40, v40, v32
	v_mov_b32_e32 v32, v37
	v_pk_mul_f32 v[32:33], v[32:33], v[56:57]
	s_nop 0
	v_mul_f32_e32 v34, 0xbfb8aa3b, v33
	v_exp_f32_e32 v34, v34
	s_nop 0
	v_add_f32_e32 v34, 1.0, v34
	v_rcp_f32_e32 v34, v34
	s_nop 0
	v_mul_f32_e32 v33, v33, v34
	v_mul_f32_e32 v37, v32, v33
	v_pk_mul_f32 v[32:33], v[48:49], v[56:57]
	s_nop 0
	v_mul_f32_e32 v34, 0xbfb8aa3b, v33
; __device__ __forceinline__ float fast_sigmoid(float x) { return __builtin_amdgcn_rcpf(1.f + __builtin_amdgcn_exp2f(-LOG2E * x)); }
;     __device__ __forceinline__ void operator()(const f32x4 (&acc)[2][2][4][2], const Unit& u, int wr, int wc, int fr, int fq, const float* pre = nullptr) const {
;     ...
;         for (int ai = 0; ai < 2; ++ai)
; #pragma unroll
;             for (int m = 0; m < 4; ++m) { const int row = EPI_ROWS(ai, m); const float rs = rs8[ai][m], gw = gw8[ai][m];
;                 const float rs2 = rs * gw; f32x4 o[2];
; #pragma unroll
;                 for (int bj = 0; bj < 2; ++bj)
; #pragma unroll
;                     for (int e = 0; e < 4; ++e) { const float a = acc[ai][bj][m][0][e] * rs, b = acc[ai][bj][m][1][e] * rs2; o[bj][e] = a * fast_sigmoid(a) * b; }
;                 if ((MOE && MOE_FP8) || (!MOE && f8)) { u32x2 w; w.x = pk4_fp8(o[0][0], o[0][1], o[0][2], o[0][3]); w.y = pk4_fp8(o[1][0], o[1][1], o[1][2], o[1][3]);
;                     *(u32x2*)((unsigned char*)G + (size_t)row * DFF + u.pn * HALF + wc * 32 + 8 * fq) = w; }
	v_exp_f32_e32 v34, v34
	s_nop 0
	v_add_f32_e32 v34, 1.0, v34
	v_rcp_f32_e32 v34, v34
	s_nop 0
	v_mul_f32_e32 v33, v33, v34
	v_mov_b32_e32 v34, v39
	v_mul_f32_e32 v41, v32, v33
	v_pk_mul_f32 v[32:33], v[34:35], v[56:57]
	v_med3_f32 v35, v44, s49, v254
	v_mul_f32_e32 v34, 0xbfb8aa3b, v33
	v_exp_f32_e32 v34, v34
	v_mov_b32_e32 v39, v24
	v_mov_b32_e32 v24, v29
	v_add_f32_e32 v34, 1.0, v34
	v_rcp_f32_e32 v34, v34
	s_nop 0
	v_mul_f32_e32 v33, v33, v34
	v_mul_f32_e32 v34, v32, v33
	v_med3_f32 v32, v36, s49, v254
	v_med3_f32 v33, v38, s49, v254
	v_cvt_pk_fp8_f32 v32, v32, v33
	v_med3_f32 v36, v42, s49, v254
	v_med3_f32 v33, v40, s49, v254
	v_med3_f32 v34, v34, s49, v254
	v_cvt_pk_fp8_f32 v32, v35, v36 op_sel:[0,0,1]
	v_med3_f32 v35, v37, s49, v254
	v_cvt_pk_fp8_f32 v33, v33, v35
	v_med3_f32 v36, v41, s49, v254
	v_mul_f32_e32 v41, 0x3c800000, v135
	v_mov_b32_e32 v38, v28
	v_cvt_pk_fp8_f32 v33, v36, v34 op_sel:[0,0,1]
	v_mad_i64_i32 v[34:35], s[54:55], v136, s58, v[112:113]
	v_lshl_add_u64 v[34:35], v[34:35], 0, s[6:7]
	v_lshl_add_u64 v[34:35], v[34:35], 0, s[12:13]
	v_mul_f32_e32 v40, 0x41000000, v41
	v_lshl_add_u64 v[34:35], v[34:35], 0, v[128:129]
	v_pk_mul_f32 v[38:39], v[38:39], v[40:41]
	global_store_dwordx2 v[34:35], v[32:33], off
	v_mov_b32_e32 v35, v16
	v_mul_f32_e32 v16, 0xbfb8aa3b, v39
	v_exp_f32_e32 v16, v16
	v_pk_mul_f32 v[24:25], v[24:25], v[40:41]
	v_mov_b32_e32 v34, v20
	v_mov_b32_e32 v36, v30
	v_add_f32_e32 v16, 1.0, v16
	v_rcp_f32_e32 v16, v16
	v_mov_b32_e32 v37, v26
	v_mov_b32_e32 v32, v22
	v_mov_b32_e32 v26, v31
	v_mul_f32_e32 v16, v39, v16
	v_mul_f32_e32 v20, v38, v16
	v_mul_f32_e32 v16, 0xbfb8aa3b, v25
	v_exp_f32_e32 v16, v16
	v_mov_b32_e32 v33, v18
	v_add_f32_e32 v16, 1.0, v16
	v_rcp_f32_e32 v16, v16
	s_nop 0
	v_mul_f32_e32 v16, v25, v16
	v_mul_f32_e32 v22, v24, v16
	v_pk_mul_f32 v[24:25], v[36:37], v[40:41]
	s_nop 0
	v_mul_f32_e32 v16, 0xbfb8aa3b, v25
	v_exp_f32_e32 v16, v16
	s_nop 0
	v_add_f32_e32 v16, 1.0, v16
	v_rcp_f32_e32 v16, v16
	s_nop 0
	v_mul_f32_e32 v16, v25, v16
	v_mul_f32_e32 v28, v24, v16
	v_pk_mul_f32 v[24:25], v[26:27], v[40:41]
	s_nop 0
	v_mul_f32_e32 v16, 0xbfb8aa3b, v25
	v_exp_f32_e32 v16, v16
	s_nop 0
	v_add_f32_e32 v16, 1.0, v16
	v_rcp_f32_e32 v16, v16
	s_nop 0
	v_mul_f32_e32 v16, v25, v16
	v_mul_f32_e32 v26, v24, v16
	v_pk_mul_f32 v[24:25], v[34:35], v[40:41]
	s_nop 0
	v_mul_f32_e32 v16, 0xbfb8aa3b, v25
	v_exp_f32_e32 v16, v16
	s_nop 0
	v_add_f32_e32 v16, 1.0, v16
	v_rcp_f32_e32 v16, v16
	s_nop 0
	v_mul_f32_e32 v16, v25, v16
	v_mul_f32_e32 v24, v24, v16
	v_mov_b32_e32 v16, v21
	v_pk_mul_f32 v[16:17], v[16:17], v[40:41]
	s_nop 0
	v_mul_f32_e32 v18, 0xbfb8aa3b, v17
	v_exp_f32_e32 v18, v18
	s_nop 0
	v_add_f32_e32 v18, 1.0, v18
	v_rcp_f32_e32 v18, v18
	s_nop 0
	v_mul_f32_e32 v17, v17, v18
	v_mul_f32_e32 v21, v16, v17
	v_pk_mul_f32 v[16:17], v[32:33], v[40:41]
	s_nop 0
	v_mul_f32_e32 v18, 0xbfb8aa3b, v17
	v_exp_f32_e32 v18, v18
	s_nop 0
	v_add_f32_e32 v18, 1.0, v18
	v_rcp_f32_e32 v18, v18
	s_nop 0
	v_mul_f32_e32 v17, v17, v18
	v_mov_b32_e32 v18, v23
	v_mul_f32_e32 v25, v16, v17
	v_pk_mul_f32 v[16:17], v[18:19], v[40:41]
	v_med3_f32 v19, v28, s49, v254
	v_mul_f32_e32 v18, 0xbfb8aa3b, v17
	v_exp_f32_e32 v18, v18
	v_mov_b32_e32 v23, v8
	v_mov_b32_e32 v8, v13
	v_add_f32_e32 v18, 1.0, v18
	v_rcp_f32_e32 v18, v18
	s_nop 0
	v_mul_f32_e32 v17, v17, v18
	v_mul_f32_e32 v18, v16, v17
	v_med3_f32 v16, v20, s49, v254
	v_med3_f32 v17, v22, s49, v254
	v_cvt_pk_fp8_f32 v16, v16, v17
	v_med3_f32 v20, v26, s49, v254
	v_med3_f32 v17, v24, s49, v254
	v_med3_f32 v18, v18, s49, v254
	v_cvt_pk_fp8_f32 v16, v19, v20 op_sel:[0,0,1]
	v_med3_f32 v19, v21, s49, v254
	v_cvt_pk_fp8_f32 v17, v17, v19
	v_med3_f32 v20, v25, s49, v254
	v_mul_f32_e32 v25, 0x3c800000, v130
	v_mov_b32_e32 v22, v12
	v_cvt_pk_fp8_f32 v17, v20, v18 op_sel:[0,0,1]
	v_mad_i64_i32 v[18:19], s[54:55], v134, s58, v[112:113]
	v_lshl_add_u64 v[18:19], v[18:19], 0, s[6:7]
	v_lshl_add_u64 v[18:19], v[18:19], 0, s[12:13]
	v_mul_f32_e32 v24, 0x41000000, v25
	v_lshl_add_u64 v[18:19], v[18:19], 0, v[128:129]
	v_pk_mul_f32 v[22:23], v[22:23], v[24:25]
	global_store_dwordx2 v[18:19], v[16:17], off
	v_mov_b32_e32 v18, v0
	v_mul_f32_e32 v0, 0xbfb8aa3b, v23
	v_exp_f32_e32 v0, v0
	v_pk_mul_f32 v[8:9], v[8:9], v[24:25]
	v_mov_b32_e32 v16, v2
	v_mov_b32_e32 v20, v14
	v_add_f32_e32 v0, 1.0, v0
	v_rcp_f32_e32 v0, v0
	v_mov_b32_e32 v21, v10
	v_mov_b32_e32 v10, v15
	v_mov_b32_e32 v19, v4
	v_mul_f32_e32 v0, v23, v0
	v_mul_f32_e32 v2, v22, v0
	v_mul_f32_e32 v0, 0xbfb8aa3b, v9
	v_exp_f32_e32 v0, v0
	v_mov_b32_e32 v4, v1
	v_mov_b32_e32 v17, v6
	v_mov_b32_e32 v6, v3
	v_add_f32_e32 v0, 1.0, v0
	v_rcp_f32_e32 v0, v0
	s_nop 0
	v_mul_f32_e32 v0, v9, v0
	v_mul_f32_e32 v12, v8, v0
	v_pk_mul_f32 v[8:9], v[20:21], v[24:25]
	s_nop 0
	v_mul_f32_e32 v0, 0xbfb8aa3b, v9
	v_exp_f32_e32 v0, v0
	s_nop 0
	v_add_f32_e32 v0, 1.0, v0
	v_rcp_f32_e32 v0, v0
	s_nop 0
	v_mul_f32_e32 v0, v9, v0
	v_mul_f32_e32 v13, v8, v0
	v_pk_mul_f32 v[8:9], v[10:11], v[24:25]
	s_nop 0
	v_mul_f32_e32 v0, 0xbfb8aa3b, v9
	v_exp_f32_e32 v0, v0
	s_nop 0
	v_add_f32_e32 v0, 1.0, v0
	v_rcp_f32_e32 v0, v0
	s_nop 0
	v_mul_f32_e32 v0, v9, v0
	v_mul_f32_e32 v10, v8, v0
	v_pk_mul_f32 v[8:9], v[18:19], v[24:25]
	s_nop 0
	v_mul_f32_e32 v0, 0xbfb8aa3b, v9
	v_exp_f32_e32 v0, v0
	s_nop 0
	v_add_f32_e32 v0, 1.0, v0
	v_rcp_f32_e32 v0, v0
	s_nop 0
	v_mul_f32_e32 v0, v9, v0
	v_mul_f32_e32 v8, v8, v0
	v_pk_mul_f32 v[0:1], v[4:5], v[24:25]
	s_nop 0
	v_mul_f32_e32 v4, 0xbfb8aa3b, v1
	v_exp_f32_e32 v4, v4
	s_nop 0
	v_add_f32_e32 v4, 1.0, v4
	v_rcp_f32_e32 v4, v4
	s_nop 0
	v_mul_f32_e32 v1, v1, v4
	v_mul_f32_e32 v4, v0, v1
	v_pk_mul_f32 v[0:1], v[16:17], v[24:25]
	s_nop 0
	v_mul_f32_e32 v5, 0xbfb8aa3b, v1
	v_exp_f32_e32 v5, v5
	s_nop 0
	v_add_f32_e32 v5, 1.0, v5
	v_rcp_f32_e32 v5, v5
	s_nop 0
	v_mul_f32_e32 v1, v1, v5
	v_mul_f32_e32 v5, v0, v1
	v_pk_mul_f32 v[0:1], v[6:7], v[24:25]
	v_med3_f32 v6, v10, s49, v254
	v_mul_f32_e32 v3, 0xbfb8aa3b, v1
	v_exp_f32_e32 v3, v3
	s_nop 0
	v_add_f32_e32 v3, 1.0, v3
	v_rcp_f32_e32 v3, v3
	s_nop 0
	v_mul_f32_e32 v1, v1, v3
	v_mul_f32_e32 v3, v0, v1
	v_med3_f32 v0, v2, s49, v254
	v_med3_f32 v1, v12, s49, v254
	v_cvt_pk_fp8_f32 v0, v0, v1
	v_med3_f32 v2, v13, s49, v254
	v_med3_f32 v1, v8, s49, v254
	v_med3_f32 v3, v3, s49, v254
	v_cvt_pk_fp8_f32 v0, v2, v6 op_sel:[0,0,1]
	v_med3_f32 v2, v4, s49, v254
	v_cvt_pk_fp8_f32 v1, v1, v2
	v_med3_f32 v4, v5, s49, v254
	v_cvt_pk_fp8_f32 v1, v4, v3 op_sel:[0,0,1]
	v_mad_i64_i32 v[2:3], s[54:55], v132, s58, v[112:113]
	v_lshl_add_u64 v[2:3], v[2:3], 0, s[6:7]
	v_lshl_add_u64 v[2:3], v[2:3], 0, s[12:13]
	v_lshl_add_u64 v[2:3], v[2:3], 0, v[128:129]
	s_mov_b64 s[6:7], -1
	global_store_dwordx2 v[2:3], v[0:1], off
	s_cbranch_vccnz .LBB0_1776
	s_andn2_b64 vcc, exec, s[2:3]
	v_mov_b32 v0, 0
	s_cbranch_vccnz .LBB0_1775
	s_barrier
	s_branch .LBB0_1775
